# LDS-DMA issue blocks without the M0 save/restore and with one wait state (M0 has no other reader)
# baseline (speedup 1.0000x reference)
; #define LAS3 __attribute__((address_space(3)))
; #define G_WAIT_V(n) asm volatile("s_waitcnt vmcnt(" #n ")" ::: "memory")
;     ...
;     const int lane = tid & 63, wr = wid >> 2, wc = wid & 3, fr = lane & 15, fq = lane >> 4;
;     const int c0 = fq ^ (fr >> 1);
;     const int a_rd0 = (wr * 64 + fr) * 128 + c0 * 16, a_rd1 = (wr * 64 + fr) * 128 + (c0 ^ 4) * 16;
;     const int cb = BSW ? (c0 ^ (wc & 1)) : c0;
;     const int b_rd0 = (wc * 16 + fr) * 128 + cb * 16, b_rd1 = (wc * 16 + fr) * 128 + (cb ^ 4) * 16;
;     const unsigned lds_u = (unsigned)(unsigned long)lds;
;     LAS3 const char* ap0 = lds + a_rd0; LAS3 const char* ap1 = lds + a_rd1; LAS3 const char* bp0 = lds + 4 * GHTB + b_rd0; LAS3 const char* bp1 = lds + 4 * GHTB + b_rd1;
;     asm volatile("" : "+v"(ap0), "+v"(ap1), "+v"(bp0), "+v"(bp1));
;     const int dma0 = wid * 1024, dma1 = (8 + wid) * 1024;
;     const unsigned boffl = (unsigned)lane * 16u;
;     ...
;     v8i32d At[4], B0[2], B1[2];
;     if (!ACCUM)
; #pragma unroll
;     for (int ai = 0; ai < 2; ++ai)
; #pragma unroll
;         for (int bj = 0; bj < 2; ++bj)
; #pragma unroll
;             for (int m = 0; m < 4; ++m)
; #pragma unroll
;                 for (int n = 0; n < 2; ++n) acc[ai][bj][m][n] = (f32x4){0.f, 0.f, 0.f, 0.f};
;     STG_B(0, 0, 0); STG_A(0, 0, 0); STG_B(0, 1, 0); STG_A(0, 1, 0);
;     __builtin_amdgcn_s_waitcnt(0);
;     { int wr1 = wid >> 2; asm volatile("" : "+s"(wr1)); if (wr1 == 1) G_BAR; }
;     G_BAR;
;     { const int p1 = (1 < nt) ? 1 : 0; STG_B(1, 0, p1); STG_A(1, 0, p1); STG_B(1, 1, p1); }
;     G_WAIT_V(6); G_BAR;
; template <int EPI>
; __device__ __forceinline__ void gemm_tile_img(const GemmArgs& g, int pm, int pn, int e, int ebase, int ecnt, LAS3 char* lds, int wid, const unsigned char* img, const TileSync& sy, int kh = -1) {
;     ...
; #pragma unroll
;     for (int h = 0; h < 2; ++h)
; #pragma unroll
;         for (int i = 0; i < 2; ++i) {
;             const int rih = (i * 8 + wid) * 8 + (lane >> 3);
;             const int chunk = (lane & 7) ^ ((rih >> 1) & 7);
;             int r = pm * 256 + h * 128 + rih;
;             unsigned grow;
;             if (EPI == 2) { if (r >= ecnt) r = ecnt - 1; grow = (unsigned)(g.list[e * T + r] >> 2); }
;             else if (EPI == 3) { grow = (unsigned)(((g.abase >> 8) + pm) * (16 * 256) + h * 128 + rih); }
;             else grow = (unsigned)r;
.LBB0_87:
	v_mbcnt_lo_u32_b32 v0, -1, 0
	v_mbcnt_hi_u32_b32 v0, -1, v0
	s_ashr_i32 s5, s4, 31
	v_add_u32_e32 v0, s75, v0
	v_readlane_b32 s36, v254, 20
	s_lshl_b64 s[6:7], s[4:5], 20
	v_lshrrev_b32_e32 v1, 3, v0
	v_readlane_b32 s38, v254, 22
	v_and_or_b32 v1, v1, 7, s3
	v_readlane_b32 s39, v254, 23
	s_add_u32 s5, s38, s6
	v_lshrrev_b32_e32 v2, 1, v1
	s_addc_u32 s89, s39, s7
	s_lshl_b32 s1, s88, 8
	v_xor_b32_e32 v2, v2, v0
	v_add_lshl_u32 v1, v1, s1, 12
	v_lshlrev_b32_e32 v2, 4, v2
	s_cmp_lt_i32 s0, 1
	v_lshlrev_b32_e32 v3, 3, v0
	v_and_or_b32 v128, v2, s73, v1
	s_cselect_b64 s[6:7], -1, 0
	s_cmp_gt_i32 s0, 0
	v_and_b32_e32 v1, 63, v0
	v_and_b32_e32 v2, 15, v0
	v_bitop3_b32 v0, v3, v0, 63 bitop3:0x78
	s_cselect_b32 vcc_lo, 16, 0
	v_bitop3_b32 v3, v3, s73, v1 bitop3:0x48
	v_bitop3_b32 v0, v0, 64, v130 bitop3:0x6c
	v_or_b32_e32 v4, s11, v2
	v_lshl_add_u32 v2, v2, 7, s12
	s_add_i32 s1, 0, 0x10000
	v_add_u32_e32 v131, v2, v3
	v_add_u32_e32 v132, v2, v0
	v_lshl_add_u32 v2, v4, 7, s1
	s_lshl_b32 s1, vcc_lo, 15
	s_add_u32 s1, s5, s1
	s_addc_u32 s34, s89, 0
	s_add_u32 s8, s1, s13
	v_add_u32_e32 v133, v2, v3
	v_add_u32_e32 v134, v2, v0
	s_addc_u32 s9, s34, s15
	v_lshlrev_b32_e32 v135, 4, v1
	s_mov_b32 m0, s17
	s_nop 0
	global_load_lds_dwordx4 v135, s[8:9]
	s_add_u32 s8, s1, s14
	s_addc_u32 s9, s34, s18
	s_mov_b32 m0, s19
	s_nop 0
	global_load_lds_dwordx4 v135, s[8:9]
	s_lshl_b32 s8, vcc_lo, 7
	s_add_u32 s8, s54, s8
	s_addc_u32 s9, s55, 0
	s_mov_b32 m0, s16
	s_nop 0
	global_load_lds_dwordx4 v128, s[8:9]
	s_add_u32 s68, s8, 0x40000
	s_addc_u32 s69, s9, 0
	s_add_u32 s1, s1, 0x4000
	s_addc_u32 s34, s34, 0
	s_mov_b32 m0, s20
	s_nop 0
	global_load_lds_dwordx4 v128, s[68:69]
	s_add_u32 s68, s1, s13
	s_addc_u32 s69, s34, s15
	s_mov_b32 m0, s21
	s_nop 0
	global_load_lds_dwordx4 v135, s[68:69]
	s_add_u32 s68, s1, s14
	s_addc_u32 s69, s34, s18
	s_mov_b32 m0, s22
	s_nop 0
	global_load_lds_dwordx4 v135, s[68:69]
	s_add_u32 s68, s8, 0x80000
	s_addc_u32 s69, s9, 0
	s_mov_b32 m0, s23
	s_nop 0
	global_load_lds_dwordx4 v128, s[68:69]
	s_add_u32 s8, s8, 0xc0000
	s_addc_u32 s9, s9, 0
	s_mov_b32 m0, s24
	s_nop 0
	global_load_lds_dwordx4 v128, s[8:9]
	s_mov_b32 s1, s10
	s_waitcnt vmcnt(0) expcnt(0) lgkmcnt(0)
	s_cmp_lg_u32 s1, 1
	v_readlane_b32 s37, v254, 21
	v_readlane_b32 s40, v254, 24
	v_readlane_b32 s41, v254, 25
	v_readlane_b32 s42, v254, 26
	v_readlane_b32 s43, v254, 27
	v_readlane_b32 s44, v254, 28
	v_readlane_b32 s45, v254, 29
	v_readlane_b32 s46, v254, 30
	v_readlane_b32 s47, v254, 31
	v_readlane_b32 s48, v254, 32
	v_readlane_b32 s49, v254, 33
	v_readlane_b32 s50, v254, 34
	v_readlane_b32 s51, v254, 35
	s_cbranch_scc1 .LBB0_89
	s_barrier
.LBB0_89:
	s_cmp_gt_i32 s0, -1
	s_cselect_b32 s34, 16, 32
	s_or_b32 s8, vcc_lo, 1
	s_lshl_b32 s0, s8, 15
	s_add_u32 s9, s5, s0
	s_addc_u32 s68, s89, 0
	s_add_u32 s0, s9, s13
	s_barrier
	s_addc_u32 s1, s68, s15
	s_mov_b32 m0, s25
	s_nop 0
	global_load_lds_dwordx4 v135, s[0:1]
	s_add_u32 s0, s9, s14
	s_addc_u32 s1, s68, s18
	s_mov_b32 m0, s26
	s_nop 0
	global_load_lds_dwordx4 v135, s[0:1]
	s_lshl_b32 s0, s8, 7
	s_add_u32 s0, s54, s0
	s_addc_u32 s1, s55, 0
	s_mov_b32 m0, s27
	s_nop 0
	global_load_lds_dwordx4 v128, s[0:1]
	s_add_u32 s0, s0, 0x40000
	s_addc_u32 s1, s1, 0
	s_mov_b32 m0, s28
	s_nop 0
	global_load_lds_dwordx4 v128, s[0:1]
	s_add_u32 s8, s9, 0x4000
	s_addc_u32 s9, s68, 0
	s_add_u32 s0, s8, s13
	s_addc_u32 s1, s9, s15
	s_mov_b32 m0, s29
	s_nop 0
	global_load_lds_dwordx4 v135, s[0:1]
	s_add_u32 s0, s8, s14
	s_addc_u32 s1, s9, s18
	s_mov_b32 m0, s30
	s_nop 0
	global_load_lds_dwordx4 v135, s[0:1]
	s_waitcnt vmcnt(6)
	s_barrier
	v_mov_b32_e32 v0, 0
	s_add_i32 vcc_hi, s34, -1
	s_mov_b32 s0, 3
	v_mov_b32_e32 v1, v0
	v_mov_b32_e32 v2, v0
	v_mov_b32_e32 v3, v0
	v_mov_b32_e32 v4, v0
	v_mov_b32_e32 v5, v0
	v_mov_b32_e32 v6, v0
	v_mov_b32_e32 v7, v0
	v_mov_b32_e32 v8, v0
	v_mov_b32_e32 v9, v0
	v_mov_b32_e32 v10, v0
	v_mov_b32_e32 v11, v0
	v_mov_b32_e32 v16, v0
	v_mov_b32_e32 v17, v0
	v_mov_b32_e32 v18, v0
	v_mov_b32_e32 v19, v0
	v_mov_b32_e32 v24, v0
	v_mov_b32_e32 v25, v0
	v_mov_b32_e32 v26, v0
	v_mov_b32_e32 v27, v0
	v_mov_b32_e32 v32, v0
	v_mov_b32_e32 v33, v0
	v_mov_b32_e32 v34, v0
	v_mov_b32_e32 v35, v0
	v_mov_b32_e32 v40, v0
	v_mov_b32_e32 v41, v0
	v_mov_b32_e32 v42, v0
	v_mov_b32_e32 v43, v0
	v_mov_b32_e32 v48, v0
	v_mov_b32_e32 v49, v0
	v_mov_b32_e32 v50, v0
	v_mov_b32_e32 v51, v0
	v_mov_b32_e32 v12, v0
	v_mov_b32_e32 v13, v0
	v_mov_b32_e32 v14, v0
	v_mov_b32_e32 v15, v0
	v_mov_b32_e32 v20, v0
	v_mov_b32_e32 v21, v0
	v_mov_b32_e32 v22, v0
	v_mov_b32_e32 v23, v0
	v_mov_b32_e32 v28, v0
	v_mov_b32_e32 v29, v0
	v_mov_b32_e32 v30, v0
	v_mov_b32_e32 v31, v0
	v_mov_b32_e32 v36, v0
	v_mov_b32_e32 v37, v0
	v_mov_b32_e32 v38, v0
	v_mov_b32_e32 v39, v0
	v_mov_b32_e32 v44, v0
	v_mov_b32_e32 v45, v0
	v_mov_b32_e32 v46, v0
	v_mov_b32_e32 v47, v0
	v_mov_b32_e32 v52, v0
	v_mov_b32_e32 v53, v0
	v_mov_b32_e32 v54, v0
	v_mov_b32_e32 v55, v0
	v_mov_b32_e32 v56, v0
	v_mov_b32_e32 v57, v0
	v_mov_b32_e32 v58, v0
	v_mov_b32_e32 v59, v0
	v_mov_b32_e32 v60, v0
	v_mov_b32_e32 v61, v0
	v_mov_b32_e32 v62, v0
	v_mov_b32_e32 v63, v0
	v_mov_b32_e32 v64, v0
	v_mov_b32_e32 v65, v0
	v_mov_b32_e32 v66, v0
	v_mov_b32_e32 v67, v0
	v_mov_b32_e32 v68, v0
	v_mov_b32_e32 v69, v0
	v_mov_b32_e32 v70, v0
	v_mov_b32_e32 v71, v0
	v_mov_b32_e32 v72, v0
	v_mov_b32_e32 v73, v0
	v_mov_b32_e32 v74, v0
	v_mov_b32_e32 v75, v0
	v_mov_b32_e32 v80, v0
	v_mov_b32_e32 v81, v0
	v_mov_b32_e32 v82, v0
	v_mov_b32_e32 v83, v0
	v_mov_b32_e32 v88, v0
	v_mov_b32_e32 v89, v0
	v_mov_b32_e32 v90, v0
	v_mov_b32_e32 v91, v0
	v_mov_b32_e32 v96, v0
	v_mov_b32_e32 v97, v0
	v_mov_b32_e32 v98, v0
	v_mov_b32_e32 v99, v0
	v_mov_b32_e32 v104, v0
	v_mov_b32_e32 v105, v0
	v_mov_b32_e32 v106, v0
	v_mov_b32_e32 v107, v0
	v_mov_b32_e32 v112, v0
	v_mov_b32_e32 v113, v0
	v_mov_b32_e32 v114, v0
	v_mov_b32_e32 v115, v0
	v_mov_b32_e32 v76, v0
	v_mov_b32_e32 v77, v0
	v_mov_b32_e32 v78, v0
	v_mov_b32_e32 v79, v0
	v_mov_b32_e32 v84, v0
	v_mov_b32_e32 v85, v0
	v_mov_b32_e32 v86, v0
	v_mov_b32_e32 v87, v0
	v_mov_b32_e32 v92, v0
	v_mov_b32_e32 v93, v0
	v_mov_b32_e32 v94, v0
	v_mov_b32_e32 v95, v0
	v_mov_b32_e32 v100, v0
	v_mov_b32_e32 v101, v0
	v_mov_b32_e32 v102, v0
	v_mov_b32_e32 v103, v0
	v_mov_b32_e32 v108, v0
	v_mov_b32_e32 v109, v0
	v_mov_b32_e32 v110, v0
	v_mov_b32_e32 v111, v0
	v_mov_b32_e32 v116, v0
	v_mov_b32_e32 v117, v0
	v_mov_b32_e32 v118, v0
	v_mov_b32_e32 v119, v0
	v_mov_b32_e32 v120, v0
	v_mov_b32_e32 v121, v0
	v_mov_b32_e32 v122, v0
	v_mov_b32_e32 v123, v0
	v_mov_b32_e32 v124, v0
	v_mov_b32_e32 v125, v0
	v_mov_b32_e32 v126, v0
	v_mov_b32_e32 v127, v0
; #define G_WAIT_L(n) asm volatile("s_waitcnt lgkmcnt(" #n ")" ::: "memory")
; #define G_BAR do { asm volatile("" ::: "memory"); __builtin_amdgcn_s_barrier(); asm volatile("" ::: "memory"); } while (0)
; #define G_SCHED __builtin_amdgcn_sched_barrier(0)
; #define STG_A(b, h, kt) do { const unsigned char* _g = A + (size_t)KT_(kt) * ASTEP; \
;         dma16((const void*)(_g + (size_t)((h) * 128) * ROWB), ROWB ? aoff[0][0] : aoff[h][0], lds_u + SA_(b, h) + dma0); \
;         dma16((const void*)(_g + (size_t)((h) * 128 + 64) * ROWB), ROWB ? aoff[0][0] : aoff[h][1], lds_u + SA_(b, h) + dma1); } while (0)
; #define STG_B(b, h, kt) do { const unsigned char* _g = img + (size_t)KT_(kt) * 32768 + (h) * 16384; \
;         dma16((const void*)(_g + dma0), boffl, lds_u + SB_(b, h) + dma0); \
;         dma16((const void*)(_g + dma1), boffl, lds_u + SB_(b, h) + dma1); } while (0)
; #define LDA_(dst, b, h) do { _Pragma("unroll") for (int _m = 0; _m < 4; ++_m) { \
;         dst[_m].lo = *(LAS3 const i32x4d*)(ap0 + SA_(b, h) + _m * 2048); \
;         dst[_m].hi = *(LAS3 const i32x4d*)(ap1 + SA_(b, h) + _m * 2048); } } while (0)
; #define LDBF(dst, b, h) do { _Pragma("unroll") for (int _n = 0; _n < 2; ++_n) { \
;         dst[_n].lo = *(LAS3 const i32x4d*)(bp0 + (SB_(b, h) - 4 * GHTB) + _n * 8192); \
;         dst[_n].hi = *(LAS3 const i32x4d*)(bp1 + (SB_(b, h) - 4 * GHTB) + _n * 8192); } } while (0)
;     ...
;         const int t1 = (t + 1 < nt) ? t + 1 : nt - 1, t2 = (t + 2 < nt) ? t + 2 : nt - 1, t3 = (t + 3 < nt) ? t + 3 : nt - 1;
;         LDBF(B0, 0, 0); G_SCHED; LDA_(At, 0, 0); STG_A(1, 1, t1);
;         G_WAIT_L(8); G_BAR; G_WAIT_L(0); MMAD(0, 0, At, B0); G_BAR; G_SCHED;
;         LDBF(B1, 0, 1); STG_B(0, 0, t2);
;         G_BAR; G_WAIT_L(0); MMAD(0, 1, At, B1); G_BAR;
;         LDA_(At, 0, 1); STG_A(0, 0, t2);
;         G_BAR; G_WAIT_L(0); MMAD(1, 0, At, B0); G_BAR; G_SCHED;
.LBB0_90:
	ds_read_b128 v[136:139], v133
	ds_read_b128 v[140:143], v133 offset:8192
	ds_read_b128 v[144:147], v134
	ds_read_b128 v[148:151], v134 offset:8192
	s_add_i32 s1, s0, -1
	s_add_i32 s8, s0, -2
	s_min_u32 s68, s1, vcc_hi
	s_min_u32 s8, s8, vcc_hi
	s_add_i32 s8, s8, vcc_lo
	s_lshl_b32 s8, s8, 7
	s_and_b32 s8, s8, 0xf80
	ds_read_b128 v[152:155], v131
	ds_read_b128 v[156:159], v131 offset:2048
	ds_read_b128 v[160:163], v132
	ds_read_b128 v[164:167], v132 offset:2048
	ds_read_b128 v[168:171], v131 offset:4096
	ds_read_b128 v[172:175], v131 offset:6144
	ds_read_b128 v[176:179], v132 offset:4096
	ds_read_b128 v[180:183], v132 offset:6144
	s_add_u32 s69, s54, s8
	s_addc_u32 s70, s55, 0
	s_add_u32 s8, s69, 0x80000
	s_addc_u32 s9, s70, 0
	s_mov_b32 m0, s31
	s_nop 0
	global_load_lds_dwordx4 v128, s[8:9]
	s_add_u32 s8, s69, 0xc0000
	s_addc_u32 s9, s70, 0
	s_mov_b32 m0, s33
	s_nop 0
	global_load_lds_dwordx4 v128, s[8:9]
	s_waitcnt lgkmcnt(8)
	s_waitcnt vmcnt(10)
	s_barrier
	s_waitcnt lgkmcnt(0)
	s_setprio 1
	s_waitcnt lgkmcnt(7)
	v_mfma_f32_16x16x32_bf16 v[124:127], v[136:139], v[152:155], v[124:127]
	v_mfma_f32_16x16x32_bf16 v[120:123], v[140:143], v[152:155], v[120:123]
	s_waitcnt lgkmcnt(6)
	v_mfma_f32_16x16x32_bf16 v[116:119], v[136:139], v[156:159], v[116:119]
	v_mfma_f32_16x16x32_bf16 v[108:111], v[140:143], v[156:159], v[108:111]
	s_waitcnt lgkmcnt(3)
	v_mfma_f32_16x16x32_bf16 v[100:103], v[136:139], v[168:171], v[100:103]
	v_mfma_f32_16x16x32_bf16 v[92:95], v[140:143], v[168:171], v[92:95]
	s_waitcnt lgkmcnt(2)
	v_mfma_f32_16x16x32_bf16 v[84:87], v[136:139], v[172:175], v[84:87]
	v_mfma_f32_16x16x32_bf16 v[76:79], v[140:143], v[172:175], v[76:79]
	v_mfma_f32_16x16x32_bf16 v[124:127], v[144:147], v[160:163], v[124:127]
	v_mfma_f32_16x16x32_bf16 v[120:123], v[148:151], v[160:163], v[120:123]
	v_mfma_f32_16x16x32_bf16 v[116:119], v[144:147], v[164:167], v[116:119]
	v_mfma_f32_16x16x32_bf16 v[108:111], v[148:151], v[164:167], v[108:111]
	s_waitcnt lgkmcnt(1)
	v_mfma_f32_16x16x32_bf16 v[100:103], v[144:147], v[176:179], v[100:103]
	v_mfma_f32_16x16x32_bf16 v[92:95], v[148:151], v[176:179], v[92:95]
	s_waitcnt lgkmcnt(0)
	v_mfma_f32_16x16x32_bf16 v[84:87], v[144:147], v[180:183], v[84:87]
	v_mfma_f32_16x16x32_bf16 v[76:79], v[148:151], v[180:183], v[76:79]
	s_setprio 0
	s_barrier
	s_add_i32 s68, s68, vcc_lo
	s_and_b32 s68, s68, 31
	s_lshl_b32 s8, s68, 15
	s_add_u32 s70, s5, s8
	s_addc_u32 s71, s89, 0
	s_add_u32 s8, s70, s13
	ds_read_b128 v[184:187], v133 offset:16384
	ds_read_b128 v[188:191], v133 offset:24576
	ds_read_b128 v[192:195], v134 offset:16384
	ds_read_b128 v[196:199], v134 offset:24576
	s_addc_u32 s9, s71, s15
	s_mov_b32 m0, s17
	s_nop 0
	global_load_lds_dwordx4 v135, s[8:9]
	s_add_u32 s8, s70, s14
	s_addc_u32 s9, s71, s18
	s_mov_b32 m0, s19
	s_nop 0
	global_load_lds_dwordx4 v135, s[8:9]
	s_waitcnt vmcnt(10)
	s_barrier
	s_waitcnt lgkmcnt(0)
	s_setprio 1
	s_waitcnt lgkmcnt(3)
	v_mfma_f32_16x16x32_bf16 v[112:115], v[184:187], v[152:155], v[112:115]
	s_waitcnt lgkmcnt(2)
	v_mfma_f32_16x16x32_bf16 v[104:107], v[188:191], v[152:155], v[104:107]
	v_mfma_f32_16x16x32_bf16 v[96:99], v[184:187], v[156:159], v[96:99]
	v_mfma_f32_16x16x32_bf16 v[88:91], v[188:191], v[156:159], v[88:91]
	v_mfma_f32_16x16x32_bf16 v[80:83], v[184:187], v[168:171], v[80:83]
	v_mfma_f32_16x16x32_bf16 v[72:75], v[188:191], v[168:171], v[72:75]
	v_mfma_f32_16x16x32_bf16 v[68:71], v[184:187], v[172:175], v[68:71]
	v_mfma_f32_16x16x32_bf16 v[64:67], v[188:191], v[172:175], v[64:67]
	s_waitcnt lgkmcnt(1)
	v_mfma_f32_16x16x32_bf16 v[112:115], v[192:195], v[160:163], v[112:115]
	s_waitcnt lgkmcnt(0)
	v_mfma_f32_16x16x32_bf16 v[104:107], v[196:199], v[160:163], v[104:107]
	v_mfma_f32_16x16x32_bf16 v[96:99], v[192:195], v[164:167], v[96:99]
	v_mfma_f32_16x16x32_bf16 v[88:91], v[196:199], v[164:167], v[88:91]
	v_mfma_f32_16x16x32_bf16 v[80:83], v[192:195], v[176:179], v[80:83]
	v_mfma_f32_16x16x32_bf16 v[72:75], v[196:199], v[176:179], v[72:75]
	v_mfma_f32_16x16x32_bf16 v[68:71], v[192:195], v[180:183], v[68:71]
	v_mfma_f32_16x16x32_bf16 v[64:67], v[196:199], v[180:183], v[64:67]
	s_setprio 0
	s_barrier
	ds_read_b128 v[152:155], v131 offset:16384
	ds_read_b128 v[156:159], v131 offset:18432
	ds_read_b128 v[160:163], v132 offset:16384
	ds_read_b128 v[164:167], v132 offset:18432
	ds_read_b128 v[168:171], v131 offset:20480
	ds_read_b128 v[172:175], v131 offset:22528
	ds_read_b128 v[176:179], v132 offset:20480
	ds_read_b128 v[180:183], v132 offset:22528
	s_lshl_b32 s8, s68, 7
	s_add_u32 s8, s54, s8
	s_addc_u32 s9, s55, 0
	s_mov_b32 m0, s16
	s_nop 0
	global_load_lds_dwordx4 v128, s[8:9]
	s_add_u32 s68, s8, 0x40000
	s_addc_u32 s69, s9, 0
	s_mov_b32 m0, s20
	s_nop 0
	global_load_lds_dwordx4 v128, s[68:69]
	s_barrier
	s_waitcnt lgkmcnt(0)
	s_setprio 1
	s_waitcnt lgkmcnt(7)
	v_mfma_f32_16x16x32_bf16 v[60:63], v[136:139], v[152:155], v[60:63]
	v_mfma_f32_16x16x32_bf16 v[56:59], v[140:143], v[152:155], v[56:59]
	s_waitcnt lgkmcnt(6)
	v_mfma_f32_16x16x32_bf16 v[52:55], v[136:139], v[156:159], v[52:55]
	v_mfma_f32_16x16x32_bf16 v[44:47], v[140:143], v[156:159], v[44:47]
	s_waitcnt lgkmcnt(3)
	v_mfma_f32_16x16x32_bf16 v[36:39], v[136:139], v[168:171], v[36:39]
	v_mfma_f32_16x16x32_bf16 v[28:31], v[140:143], v[168:171], v[28:31]
	s_waitcnt lgkmcnt(2)
	v_mfma_f32_16x16x32_bf16 v[20:23], v[136:139], v[172:175], v[20:23]
	v_mfma_f32_16x16x32_bf16 v[12:15], v[140:143], v[172:175], v[12:15]
	v_mfma_f32_16x16x32_bf16 v[60:63], v[144:147], v[160:163], v[60:63]
	v_mfma_f32_16x16x32_bf16 v[56:59], v[148:151], v[160:163], v[56:59]
	v_mfma_f32_16x16x32_bf16 v[52:55], v[144:147], v[164:167], v[52:55]
	v_mfma_f32_16x16x32_bf16 v[44:47], v[148:151], v[164:167], v[44:47]
	s_waitcnt lgkmcnt(1)
	v_mfma_f32_16x16x32_bf16 v[36:39], v[144:147], v[176:179], v[36:39]
	v_mfma_f32_16x16x32_bf16 v[28:31], v[148:151], v[176:179], v[28:31]
	s_waitcnt lgkmcnt(0)
	v_mfma_f32_16x16x32_bf16 v[20:23], v[144:147], v[180:183], v[20:23]
	v_mfma_f32_16x16x32_bf16 v[12:15], v[148:151], v[180:183], v[12:15]
	s_setprio 0
	s_barrier
; #define G_WAIT_V(n) asm volatile("s_waitcnt vmcnt(" #n ")" ::: "memory")
; #define G_WAIT_L(n) asm volatile("s_waitcnt lgkmcnt(" #n ")" ::: "memory")
; #define G_BAR do { asm volatile("" ::: "memory"); __builtin_amdgcn_s_barrier(); asm volatile("" ::: "memory"); } while (0)
; #define G_SCHED __builtin_amdgcn_sched_barrier(0)
; #define STG_A(b, h, kt) do { const unsigned char* _g = A + (size_t)KT_(kt) * ASTEP; \
;         dma16((const void*)(_g + (size_t)((h) * 128) * ROWB), ROWB ? aoff[0][0] : aoff[h][0], lds_u + SA_(b, h) + dma0); \
;         dma16((const void*)(_g + (size_t)((h) * 128 + 64) * ROWB), ROWB ? aoff[0][0] : aoff[h][1], lds_u + SA_(b, h) + dma1); } while (0)
; #define STG_B(b, h, kt) do { const unsigned char* _g = img + (size_t)KT_(kt) * 32768 + (h) * 16384; \
;         dma16((const void*)(_g + dma0), boffl, lds_u + SB_(b, h) + dma0); \
;         dma16((const void*)(_g + dma1), boffl, lds_u + SB_(b, h) + dma1); } while (0)
; #define LDA_(dst, b, h) do { _Pragma("unroll") for (int _m = 0; _m < 4; ++_m) { \
;         dst[_m].lo = *(LAS3 const i32x4d*)(ap0 + SA_(b, h) + _m * 2048); \
;         dst[_m].hi = *(LAS3 const i32x4d*)(ap1 + SA_(b, h) + _m * 2048); } } while (0)
; #define LDBF(dst, b, h) do { _Pragma("unroll") for (int _n = 0; _n < 2; ++_n) { \
;         dst[_n].lo = *(LAS3 const i32x4d*)(bp0 + (SB_(b, h) - 4 * GHTB) + _n * 8192); \
;         dst[_n].hi = *(LAS3 const i32x4d*)(bp1 + (SB_(b, h) - 4 * GHTB) + _n * 8192); } } while (0)
;     ...
;         STG_B(0, 1, t2);
;         G_WAIT_V(6); G_BAR; MMAD(1, 1, At, B1); G_BAR;
;         LDBF(B0, 1, 0); G_SCHED; LDA_(At, 1, 0); STG_A(0, 1, t2);
;         G_WAIT_L(8); G_BAR; G_WAIT_L(0); MMAD(0, 0, At, B0); G_BAR; G_SCHED;
;         LDBF(B1, 1, 1); STG_B(1, 0, t3);
	s_add_u32 s70, s70, 0x4000
	s_addc_u32 s71, s71, 0
	s_add_u32 s68, s70, s13
	s_addc_u32 s69, s71, s15
	s_mov_b32 m0, s21
	s_nop 0
	global_load_lds_dwordx4 v135, s[68:69]
	s_add_u32 s68, s70, s14
	s_addc_u32 s69, s71, s18
	s_mov_b32 m0, s22
	s_nop 0
	global_load_lds_dwordx4 v135, s[68:69]
	s_waitcnt vmcnt(10)
	s_barrier
	s_setprio 1
	v_mfma_f32_16x16x32_bf16 v[48:51], v[184:187], v[152:155], v[48:51]
	v_mfma_f32_16x16x32_bf16 v[40:43], v[188:191], v[152:155], v[40:43]
	v_mfma_f32_16x16x32_bf16 v[32:35], v[184:187], v[156:159], v[32:35]
	v_mfma_f32_16x16x32_bf16 v[24:27], v[188:191], v[156:159], v[24:27]
	v_mfma_f32_16x16x32_bf16 v[16:19], v[184:187], v[168:171], v[16:19]
	v_mfma_f32_16x16x32_bf16 v[8:11], v[188:191], v[168:171], v[8:11]
	v_mfma_f32_16x16x32_bf16 v[4:7], v[184:187], v[172:175], v[4:7]
	v_mfma_f32_16x16x32_bf16 v[0:3], v[188:191], v[172:175], v[0:3]
	v_mfma_f32_16x16x32_bf16 v[48:51], v[192:195], v[160:163], v[48:51]
	v_mfma_f32_16x16x32_bf16 v[40:43], v[196:199], v[160:163], v[40:43]
	v_mfma_f32_16x16x32_bf16 v[32:35], v[192:195], v[164:167], v[32:35]
	v_mfma_f32_16x16x32_bf16 v[24:27], v[196:199], v[164:167], v[24:27]
	v_mfma_f32_16x16x32_bf16 v[16:19], v[192:195], v[176:179], v[16:19]
	v_mfma_f32_16x16x32_bf16 v[8:11], v[196:199], v[176:179], v[8:11]
	v_mfma_f32_16x16x32_bf16 v[4:7], v[192:195], v[180:183], v[4:7]
	v_mfma_f32_16x16x32_bf16 v[0:3], v[196:199], v[180:183], v[0:3]
	s_setprio 0
	s_barrier
	ds_read_b128 v[136:139], v133 offset:32768
	ds_read_b128 v[140:143], v133 offset:40960
	ds_read_b128 v[144:147], v134 offset:32768
	ds_read_b128 v[148:151], v134 offset:40960
	ds_read_b128 v[152:155], v131 offset:32768
	ds_read_b128 v[156:159], v131 offset:34816
	ds_read_b128 v[160:163], v132 offset:32768
	ds_read_b128 v[164:167], v132 offset:34816
	ds_read_b128 v[168:171], v131 offset:36864
	ds_read_b128 v[172:175], v131 offset:38912
	ds_read_b128 v[176:179], v132 offset:36864
	ds_read_b128 v[180:183], v132 offset:38912
	s_add_u32 s68, s8, 0x80000
	s_addc_u32 s69, s9, 0
	s_mov_b32 m0, s23
	s_nop 0
	global_load_lds_dwordx4 v128, s[68:69]
	s_add_u32 s8, s8, 0xc0000
	s_addc_u32 s9, s9, 0
	s_mov_b32 m0, s24
	s_nop 0
	global_load_lds_dwordx4 v128, s[8:9]
	s_waitcnt lgkmcnt(8)
	s_waitcnt vmcnt(10)
	s_barrier
	s_waitcnt lgkmcnt(0)
	s_setprio 1
	s_waitcnt lgkmcnt(7)
	v_mfma_f32_16x16x32_bf16 v[124:127], v[136:139], v[152:155], v[124:127]
	v_mfma_f32_16x16x32_bf16 v[120:123], v[140:143], v[152:155], v[120:123]
	s_waitcnt lgkmcnt(6)
	v_mfma_f32_16x16x32_bf16 v[116:119], v[136:139], v[156:159], v[116:119]
	v_mfma_f32_16x16x32_bf16 v[108:111], v[140:143], v[156:159], v[108:111]
	s_waitcnt lgkmcnt(3)
	v_mfma_f32_16x16x32_bf16 v[100:103], v[136:139], v[168:171], v[100:103]
	v_mfma_f32_16x16x32_bf16 v[92:95], v[140:143], v[168:171], v[92:95]
	s_waitcnt lgkmcnt(2)
	v_mfma_f32_16x16x32_bf16 v[84:87], v[136:139], v[172:175], v[84:87]
	v_mfma_f32_16x16x32_bf16 v[76:79], v[140:143], v[172:175], v[76:79]
	v_mfma_f32_16x16x32_bf16 v[124:127], v[144:147], v[160:163], v[124:127]
	v_mfma_f32_16x16x32_bf16 v[120:123], v[148:151], v[160:163], v[120:123]
	v_mfma_f32_16x16x32_bf16 v[116:119], v[144:147], v[164:167], v[116:119]
	v_mfma_f32_16x16x32_bf16 v[108:111], v[148:151], v[164:167], v[108:111]
	s_waitcnt lgkmcnt(1)
	v_mfma_f32_16x16x32_bf16 v[100:103], v[144:147], v[176:179], v[100:103]
	v_mfma_f32_16x16x32_bf16 v[92:95], v[148:151], v[176:179], v[92:95]
	s_waitcnt lgkmcnt(0)
	v_mfma_f32_16x16x32_bf16 v[84:87], v[144:147], v[180:183], v[84:87]
	v_mfma_f32_16x16x32_bf16 v[76:79], v[148:151], v[180:183], v[76:79]
	s_setprio 0
	s_barrier
	s_min_u32 s8, s0, vcc_hi
	s_add_i32 s8, s8, vcc_lo
	s_and_b32 s68, s8, 31
	s_lshl_b32 s8, s68, 15
	s_add_u32 s69, s5, s8
	s_addc_u32 s70, s89, 0
	s_add_u32 s8, s69, s13
	ds_read_b128 v[184:187], v133 offset:49152
	ds_read_b128 v[188:191], v133 offset:57344
	ds_read_b128 v[192:195], v134 offset:49152
	ds_read_b128 v[196:199], v134 offset:57344
	s_addc_u32 s9, s70, s15
	s_mov_b32 m0, s25
	s_nop 0
	global_load_lds_dwordx4 v135, s[8:9]
	s_add_u32 s8, s69, s14
	s_addc_u32 s9, s70, s18
	s_mov_b32 m0, s26
	s_nop 0
	global_load_lds_dwordx4 v135, s[8:9]
	s_waitcnt vmcnt(10)
	s_barrier
; #define G_WAIT_V(n) asm volatile("s_waitcnt vmcnt(" #n ")" ::: "memory")
; #define G_WAIT_L(n) asm volatile("s_waitcnt lgkmcnt(" #n ")" ::: "memory")
; #define G_BAR do { asm volatile("" ::: "memory"); __builtin_amdgcn_s_barrier(); asm volatile("" ::: "memory"); } while (0)
; #define G_SCHED __builtin_amdgcn_sched_barrier(0)
; #define STG_A(b, h, kt) do { const unsigned char* _g = A + (size_t)KT_(kt) * ASTEP; \
;         dma16((const void*)(_g + (size_t)((h) * 128) * ROWB), ROWB ? aoff[0][0] : aoff[h][0], lds_u + SA_(b, h) + dma0); \
;         dma16((const void*)(_g + (size_t)((h) * 128 + 64) * ROWB), ROWB ? aoff[0][0] : aoff[h][1], lds_u + SA_(b, h) + dma1); } while (0)
; #define STG_B(b, h, kt) do { const unsigned char* _g = img + (size_t)KT_(kt) * 32768 + (h) * 16384; \
;         dma16((const void*)(_g + dma0), boffl, lds_u + SB_(b, h) + dma0); \
;         dma16((const void*)(_g + dma1), boffl, lds_u + SB_(b, h) + dma1); } while (0)
; #define LDA_(dst, b, h) do { _Pragma("unroll") for (int _m = 0; _m < 4; ++_m) { \
;         dst[_m].lo = *(LAS3 const i32x4d*)(ap0 + SA_(b, h) + _m * 2048); \
;         dst[_m].hi = *(LAS3 const i32x4d*)(ap1 + SA_(b, h) + _m * 2048); } } while (0)
;     ...
;         G_BAR; G_WAIT_L(0); MMAD(0, 1, At, B1); G_BAR;
;         LDA_(At, 1, 1); STG_A(1, 0, t3);
;         G_BAR; G_WAIT_L(0); MMAD(1, 0, At, B0); G_BAR; G_SCHED;
;         STG_B(1, 1, t3);
;         G_WAIT_V(6); G_BAR; MMAD(1, 1, At, B1); G_BAR;
;     }
;     G_WAIT_V(0); G_WAIT_L(0);
;     { int wr0 = wid >> 2; asm volatile("" : "+s"(wr0)); if (wr0 == 0) G_BAR; }
;     G_BAR;
	s_waitcnt lgkmcnt(0)
	s_setprio 1
	s_waitcnt lgkmcnt(3)
	v_mfma_f32_16x16x32_bf16 v[112:115], v[184:187], v[152:155], v[112:115]
	s_waitcnt lgkmcnt(2)
	v_mfma_f32_16x16x32_bf16 v[104:107], v[188:191], v[152:155], v[104:107]
	v_mfma_f32_16x16x32_bf16 v[96:99], v[184:187], v[156:159], v[96:99]
	v_mfma_f32_16x16x32_bf16 v[88:91], v[188:191], v[156:159], v[88:91]
	v_mfma_f32_16x16x32_bf16 v[80:83], v[184:187], v[168:171], v[80:83]
	v_mfma_f32_16x16x32_bf16 v[72:75], v[188:191], v[168:171], v[72:75]
	v_mfma_f32_16x16x32_bf16 v[68:71], v[184:187], v[172:175], v[68:71]
	v_mfma_f32_16x16x32_bf16 v[64:67], v[188:191], v[172:175], v[64:67]
	s_waitcnt lgkmcnt(1)
	v_mfma_f32_16x16x32_bf16 v[112:115], v[192:195], v[160:163], v[112:115]
	s_waitcnt lgkmcnt(0)
	v_mfma_f32_16x16x32_bf16 v[104:107], v[196:199], v[160:163], v[104:107]
	v_mfma_f32_16x16x32_bf16 v[96:99], v[192:195], v[164:167], v[96:99]
	v_mfma_f32_16x16x32_bf16 v[88:91], v[196:199], v[164:167], v[88:91]
	v_mfma_f32_16x16x32_bf16 v[80:83], v[192:195], v[176:179], v[80:83]
	v_mfma_f32_16x16x32_bf16 v[72:75], v[196:199], v[176:179], v[72:75]
	v_mfma_f32_16x16x32_bf16 v[68:71], v[192:195], v[180:183], v[68:71]
	v_mfma_f32_16x16x32_bf16 v[64:67], v[196:199], v[180:183], v[64:67]
	s_setprio 0
	s_barrier
	ds_read_b128 v[152:155], v131 offset:49152
	ds_read_b128 v[156:159], v131 offset:51200
	ds_read_b128 v[160:163], v132 offset:49152
	ds_read_b128 v[164:167], v132 offset:51200
	ds_read_b128 v[168:171], v131 offset:53248
	ds_read_b128 v[172:175], v131 offset:55296
	ds_read_b128 v[176:179], v132 offset:53248
	ds_read_b128 v[180:183], v132 offset:55296
	s_lshl_b32 s8, s68, 7
	s_add_u32 s8, s54, s8
	s_addc_u32 s9, s55, 0
	s_mov_b32 m0, s27
	s_nop 0
	global_load_lds_dwordx4 v128, s[8:9]
	s_add_u32 s8, s8, 0x40000
	s_addc_u32 s9, s9, 0
	s_mov_b32 m0, s28
	s_nop 0
	global_load_lds_dwordx4 v128, s[8:9]
	s_barrier
	s_waitcnt lgkmcnt(0)
	s_setprio 1
	s_waitcnt lgkmcnt(7)
	v_mfma_f32_16x16x32_bf16 v[60:63], v[136:139], v[152:155], v[60:63]
	v_mfma_f32_16x16x32_bf16 v[56:59], v[140:143], v[152:155], v[56:59]
	s_waitcnt lgkmcnt(6)
	v_mfma_f32_16x16x32_bf16 v[52:55], v[136:139], v[156:159], v[52:55]
	v_mfma_f32_16x16x32_bf16 v[44:47], v[140:143], v[156:159], v[44:47]
	s_waitcnt lgkmcnt(3)
	v_mfma_f32_16x16x32_bf16 v[36:39], v[136:139], v[168:171], v[36:39]
	v_mfma_f32_16x16x32_bf16 v[28:31], v[140:143], v[168:171], v[28:31]
	s_waitcnt lgkmcnt(2)
	v_mfma_f32_16x16x32_bf16 v[20:23], v[136:139], v[172:175], v[20:23]
	v_mfma_f32_16x16x32_bf16 v[12:15], v[140:143], v[172:175], v[12:15]
	v_mfma_f32_16x16x32_bf16 v[60:63], v[144:147], v[160:163], v[60:63]
	v_mfma_f32_16x16x32_bf16 v[56:59], v[148:151], v[160:163], v[56:59]
	v_mfma_f32_16x16x32_bf16 v[52:55], v[144:147], v[164:167], v[52:55]
	v_mfma_f32_16x16x32_bf16 v[44:47], v[148:151], v[164:167], v[44:47]
	s_waitcnt lgkmcnt(1)
	v_mfma_f32_16x16x32_bf16 v[36:39], v[144:147], v[176:179], v[36:39]
	v_mfma_f32_16x16x32_bf16 v[28:31], v[148:151], v[176:179], v[28:31]
	s_waitcnt lgkmcnt(0)
	v_mfma_f32_16x16x32_bf16 v[20:23], v[144:147], v[180:183], v[20:23]
	v_mfma_f32_16x16x32_bf16 v[12:15], v[148:151], v[180:183], v[12:15]
	s_setprio 0
	s_barrier
	s_add_u32 s68, s69, 0x4000
	s_addc_u32 s69, s70, 0
	s_add_u32 s8, s68, s13
	s_addc_u32 s9, s69, s15
	s_mov_b32 m0, s29
	s_nop 0
	global_load_lds_dwordx4 v135, s[8:9]
	s_add_u32 s8, s68, s14
	s_addc_u32 s9, s69, s18
	s_mov_b32 m0, s30
	s_nop 0
	global_load_lds_dwordx4 v135, s[8:9]
	s_waitcnt vmcnt(10)
	s_barrier
	s_setprio 1
	v_mfma_f32_16x16x32_bf16 v[48:51], v[184:187], v[152:155], v[48:51]
	v_mfma_f32_16x16x32_bf16 v[40:43], v[188:191], v[152:155], v[40:43]
	v_mfma_f32_16x16x32_bf16 v[32:35], v[184:187], v[156:159], v[32:35]
	v_mfma_f32_16x16x32_bf16 v[24:27], v[188:191], v[156:159], v[24:27]
	v_mfma_f32_16x16x32_bf16 v[16:19], v[184:187], v[168:171], v[16:19]
	v_mfma_f32_16x16x32_bf16 v[8:11], v[188:191], v[168:171], v[8:11]
	v_mfma_f32_16x16x32_bf16 v[4:7], v[184:187], v[172:175], v[4:7]
	v_mfma_f32_16x16x32_bf16 v[0:3], v[188:191], v[172:175], v[0:3]
	v_mfma_f32_16x16x32_bf16 v[48:51], v[192:195], v[160:163], v[48:51]
	v_mfma_f32_16x16x32_bf16 v[40:43], v[196:199], v[160:163], v[40:43]
	v_mfma_f32_16x16x32_bf16 v[32:35], v[192:195], v[164:167], v[32:35]
	v_mfma_f32_16x16x32_bf16 v[24:27], v[196:199], v[164:167], v[24:27]
	v_mfma_f32_16x16x32_bf16 v[16:19], v[192:195], v[176:179], v[16:19]
	v_mfma_f32_16x16x32_bf16 v[8:11], v[196:199], v[176:179], v[8:11]
	v_mfma_f32_16x16x32_bf16 v[4:7], v[192:195], v[180:183], v[4:7]
	v_mfma_f32_16x16x32_bf16 v[0:3], v[196:199], v[180:183], v[0:3]
	s_setprio 0
	s_barrier
	s_add_i32 s0, s0, 2
	s_cmp_ge_u32 s1, s34
	s_cbranch_scc0 .LBB0_90
	s_waitcnt vmcnt(0)
	s_waitcnt lgkmcnt(0)
	s_mov_b32 s0, s10
	s_cmp_eq_u32 s0, 0
	s_cbranch_scc0 .LBB0_93
	s_barrier

; #define LAS3 __attribute__((address_space(3)))
; #define G_WAIT_V(n) asm volatile("s_waitcnt vmcnt(" #n ")" ::: "memory")
; #define G_BAR do { asm volatile("" ::: "memory"); __builtin_amdgcn_s_barrier(); asm volatile("" ::: "memory"); } while (0)
; #define STG_B(b, h, kt) do { const unsigned char* _g = img + (size_t)KT_(kt) * 32768 + (h) * 16384; \
;         dma16((const void*)(_g + dma0), boffl, lds_u + SB_(b, h) + dma0); \
;         dma16((const void*)(_g + dma1), boffl, lds_u + SB_(b, h) + dma1); } while (0)
;     ...
;     const int lane = tid & 63, wr = wid >> 2, wc = wid & 3, fr = lane & 15, fq = lane >> 4;
;     const int c0 = fq ^ (fr >> 1);
;     const int a_rd0 = (wr * 64 + fr) * 128 + c0 * 16, a_rd1 = (wr * 64 + fr) * 128 + (c0 ^ 4) * 16;
;     const int cb = BSW ? (c0 ^ (wc & 1)) : c0;
;     const int b_rd0 = (wc * 16 + fr) * 128 + cb * 16, b_rd1 = (wc * 16 + fr) * 128 + (cb ^ 4) * 16;
;     const unsigned lds_u = (unsigned)(unsigned long)lds;
;     LAS3 const char* ap0 = lds + a_rd0; LAS3 const char* ap1 = lds + a_rd1; LAS3 const char* bp0 = lds + 4 * GHTB + b_rd0; LAS3 const char* bp1 = lds + 4 * GHTB + b_rd1;
;     asm volatile("" : "+v"(ap0), "+v"(ap1), "+v"(bp0), "+v"(bp1));
;     const int dma0 = wid * 1024, dma1 = (8 + wid) * 1024;
;     const unsigned boffl = (unsigned)lane * 16u;
;     ...
;     v8i32d At[4], B0[2], B1[2];
;     if (!ACCUM)
; #pragma unroll
;     for (int ai = 0; ai < 2; ++ai)
; #pragma unroll
;         for (int bj = 0; bj < 2; ++bj)
; #pragma unroll
;             for (int m = 0; m < 4; ++m)
; #pragma unroll
;                 for (int n = 0; n < 2; ++n) acc[ai][bj][m][n] = (f32x4){0.f, 0.f, 0.f, 0.f};
;     STG_B(0, 0, 0); STG_A(0, 0, 0); STG_B(0, 1, 0); STG_A(0, 1, 0);
;     __builtin_amdgcn_s_waitcnt(0);
;     { int wr1 = wid >> 2; asm volatile("" : "+s"(wr1)); if (wr1 == 1) G_BAR; }
;     G_BAR;
;     { const int p1 = (1 < nt) ? 1 : 0; STG_B(1, 0, p1); STG_A(1, 0, p1); STG_B(1, 1, p1); }
;     G_WAIT_V(6); G_BAR;
; __global__ void __launch_bounds__(512, 2) k_mega(Params p) {
;     ...
;       for (int u = vb; u < 32 * 8; u += nb) { int pm = u & 31, pn = u >> 5;
;           if (nb == 256) { const int x = (u >> 5) & 7, j = u & 31; pm = 8 * (x & 3) + (j & 7); pn = 4 * (x >> 2) + (j >> 3); }
;           gemm_tile_img<1>(g, pm, pn, 0, 0, T, lds, wid, p.img_out + (size_t)pn * 1048576, TileSync{}); } }
.LBB0_275:
	s_ashr_i32 s17, s35, 5
	s_lshl_b32 s14, s17, 3
	s_and_b32 s14, s14, 24
	s_and_b32 s15, s35, 7
	s_or_b32 s26, s14, s15
	s_and_b32 s14, s17, 4
	s_bfe_u32 s15, s35, 0x20003
	s_and_b32 s16, s35, 31
	s_or_b32 s27, s14, s15
	s_and_b64 s[14:15], s[0:1], exec
	v_mbcnt_lo_u32_b32 v0, -1, 0
	v_mbcnt_hi_u32_b32 v0, -1, v0
	s_cselect_b32 s14, s27, s17
	v_add_u32_e32 v0, s75, v0
	s_cselect_b32 s26, s26, s16
	s_ashr_i32 s15, s14, 31
	s_lshl_b64 s[16:17], s[14:15], 20
	v_lshrrev_b32_e32 v1, 3, v0
	v_and_or_b32 v1, v1, 7, s2
	s_add_u32 s88, s40, s16
	v_lshrrev_b32_e32 v2, 1, v1
	s_addc_u32 s89, s41, s17
	s_lshl_b32 s15, s26, 8
	v_xor_b32_e32 v2, v2, v0
	v_add_lshl_u32 v1, v1, s15, 12
	v_lshlrev_b32_e32 v2, 4, v2
	v_lshlrev_b32_e32 v3, 3, v0
	v_and_or_b32 v128, v2, s87, v1
	v_and_b32_e32 v1, 63, v0
	v_and_b32_e32 v2, 15, v0
	v_bitop3_b32 v0, v3, v0, 63 bitop3:0x78
	v_bitop3_b32 v3, v3, s87, v1 bitop3:0x48
	v_bitop3_b32 v0, v0, 64, v130 bitop3:0x6c
	v_or_b32_e32 v4, s18, v2
	v_lshl_add_u32 v2, v2, 7, s19
	s_add_i32 s16, 0, 0x10000
	v_add_u32_e32 v129, v2, v3
	v_add_u32_e32 v131, v2, v0
	v_lshl_add_u32 v2, v4, 7, s16
	s_add_u32 s16, s88, s20
	v_add_u32_e32 v132, v2, v3
	v_add_u32_e32 v133, v2, v0
	s_addc_u32 s17, s89, s22
	v_lshlrev_b32_e32 v134, 4, v1
	s_mov_b32 m0, s25
	s_nop 0
	global_load_lds_dwordx4 v134, s[16:17]
	s_add_u32 s16, s88, s21
	s_addc_u32 s17, s89, s28
	s_mov_b32 m0, s29
	s_nop 0
	global_load_lds_dwordx4 v134, s[16:17]
	s_mov_b32 m0, s23
	s_nop 0
	global_load_lds_dwordx4 v128, s[60:61]
	s_add_u32 s26, s88, 0x4000
	s_mov_b32 m0, s30
	s_nop 0
	global_load_lds_dwordx4 v128, s[4:5]
	s_addc_u32 s27, s89, 0
	s_add_u32 s16, s26, s20
	s_addc_u32 s17, s27, s22
	s_mov_b32 m0, s31
	s_nop 0
	global_load_lds_dwordx4 v134, s[16:17]
	s_add_u32 s16, s26, s21
	s_addc_u32 s17, s27, s28
	s_mov_b32 m0, s33
	s_nop 0
	global_load_lds_dwordx4 v134, s[16:17]
	s_mov_b32 m0, s34
	s_nop 0
	global_load_lds_dwordx4 v128, s[6:7]
	s_nop 0
	s_mov_b32 m0, s54
	s_nop 0
	global_load_lds_dwordx4 v128, s[8:9]
	s_mov_b32 s16, s3
	s_waitcnt vmcnt(0) expcnt(0) lgkmcnt(0)
	s_cmp_lg_u32 s16, 1
	s_cbranch_scc1 .LBB0_277
	s_barrier
.LBB0_277:
	s_add_u32 s26, s88, 0x8000
	s_addc_u32 s27, s89, 0
	s_add_u32 s16, s26, s20
	s_barrier
	s_addc_u32 s17, s27, s22
	s_mov_b32 m0, s55
	s_nop 0
	global_load_lds_dwordx4 v134, s[16:17]
	s_add_u32 s16, s26, s21
	s_addc_u32 s17, s27, s28
	s_mov_b32 m0, s56
	s_nop 0
	global_load_lds_dwordx4 v134, s[16:17]
	s_mov_b32 m0, s57
	s_nop 0
	global_load_lds_dwordx4 v128, s[10:11]
	s_add_u32 s26, s88, 0xc000
	s_mov_b32 m0, s58
	s_nop 0
	global_load_lds_dwordx4 v128, s[12:13]
	s_addc_u32 s27, s89, 0
	s_add_u32 s16, s26, s20
	s_addc_u32 s17, s27, s22
	s_mov_b32 m0, s59
	s_nop 0
	global_load_lds_dwordx4 v134, s[16:17]
	s_add_u32 s16, s26, s21
	s_addc_u32 s17, s27, s28
	s_mov_b32 m0, s70
	s_nop 0
	global_load_lds_dwordx4 v134, s[16:17]
	s_waitcnt vmcnt(6)
	s_barrier
	v_mov_b32_e32 v0, 0
	s_mov_b32 s26, -2
	s_mov_b64 s[16:17], s[60:61]
	v_mov_b32_e32 v1, v0
	v_mov_b32_e32 v2, v0
	v_mov_b32_e32 v3, v0
	v_mov_b32_e32 v4, v0
	v_mov_b32_e32 v5, v0
	v_mov_b32_e32 v6, v0
	v_mov_b32_e32 v7, v0
	v_mov_b32_e32 v8, v0
	v_mov_b32_e32 v9, v0
	v_mov_b32_e32 v10, v0
	v_mov_b32_e32 v11, v0
	v_mov_b32_e32 v20, v0
	v_mov_b32_e32 v21, v0
	v_mov_b32_e32 v22, v0
	v_mov_b32_e32 v23, v0
	v_mov_b32_e32 v24, v0
	v_mov_b32_e32 v25, v0
	v_mov_b32_e32 v26, v0
	v_mov_b32_e32 v27, v0
	v_mov_b32_e32 v36, v0
	v_mov_b32_e32 v37, v0
	v_mov_b32_e32 v38, v0
	v_mov_b32_e32 v39, v0
	v_mov_b32_e32 v40, v0
	v_mov_b32_e32 v41, v0
	v_mov_b32_e32 v42, v0
	v_mov_b32_e32 v43, v0
	v_mov_b32_e32 v52, v0
	v_mov_b32_e32 v53, v0
	v_mov_b32_e32 v54, v0
	v_mov_b32_e32 v55, v0
	v_mov_b32_e32 v12, v0
	v_mov_b32_e32 v13, v0
	v_mov_b32_e32 v14, v0
	v_mov_b32_e32 v15, v0
	v_mov_b32_e32 v16, v0
	v_mov_b32_e32 v17, v0
	v_mov_b32_e32 v18, v0
	v_mov_b32_e32 v19, v0
	v_mov_b32_e32 v28, v0
	v_mov_b32_e32 v29, v0
	v_mov_b32_e32 v30, v0
	v_mov_b32_e32 v31, v0
	v_mov_b32_e32 v32, v0
	v_mov_b32_e32 v33, v0
	v_mov_b32_e32 v34, v0
	v_mov_b32_e32 v35, v0
	v_mov_b32_e32 v44, v0
	v_mov_b32_e32 v45, v0
	v_mov_b32_e32 v46, v0
	v_mov_b32_e32 v47, v0
	v_mov_b32_e32 v48, v0
	v_mov_b32_e32 v49, v0
	v_mov_b32_e32 v50, v0
	v_mov_b32_e32 v51, v0
	v_mov_b32_e32 v56, v0
	v_mov_b32_e32 v57, v0
	v_mov_b32_e32 v58, v0
	v_mov_b32_e32 v59, v0
	v_mov_b32_e32 v60, v0
	v_mov_b32_e32 v61, v0
	v_mov_b32_e32 v62, v0
	v_mov_b32_e32 v63, v0
	v_mov_b32_e32 v64, v0
	v_mov_b32_e32 v65, v0
	v_mov_b32_e32 v66, v0
	v_mov_b32_e32 v67, v0
	v_mov_b32_e32 v68, v0
	v_mov_b32_e32 v69, v0
	v_mov_b32_e32 v70, v0
	v_mov_b32_e32 v71, v0
	v_mov_b32_e32 v72, v0
	v_mov_b32_e32 v73, v0
	v_mov_b32_e32 v74, v0
	v_mov_b32_e32 v75, v0
	v_mov_b32_e32 v84, v0
	v_mov_b32_e32 v85, v0
	v_mov_b32_e32 v86, v0
	v_mov_b32_e32 v87, v0
	v_mov_b32_e32 v88, v0
	v_mov_b32_e32 v89, v0
	v_mov_b32_e32 v90, v0
	v_mov_b32_e32 v91, v0
	v_mov_b32_e32 v100, v0
	v_mov_b32_e32 v101, v0
	v_mov_b32_e32 v102, v0
	v_mov_b32_e32 v103, v0
	v_mov_b32_e32 v104, v0
	v_mov_b32_e32 v105, v0
	v_mov_b32_e32 v106, v0
	v_mov_b32_e32 v107, v0
	v_mov_b32_e32 v116, v0
	v_mov_b32_e32 v117, v0
	v_mov_b32_e32 v118, v0
	v_mov_b32_e32 v119, v0
	v_mov_b32_e32 v76, v0
	v_mov_b32_e32 v77, v0
	v_mov_b32_e32 v78, v0
	v_mov_b32_e32 v79, v0
	v_mov_b32_e32 v80, v0
	v_mov_b32_e32 v81, v0
	v_mov_b32_e32 v82, v0
	v_mov_b32_e32 v83, v0
	v_mov_b32_e32 v92, v0
	v_mov_b32_e32 v93, v0
	v_mov_b32_e32 v94, v0
	v_mov_b32_e32 v95, v0
	v_mov_b32_e32 v96, v0
	v_mov_b32_e32 v97, v0
	v_mov_b32_e32 v98, v0
	v_mov_b32_e32 v99, v0
	v_mov_b32_e32 v108, v0
	v_mov_b32_e32 v109, v0
	v_mov_b32_e32 v110, v0
	v_mov_b32_e32 v111, v0
	v_mov_b32_e32 v112, v0
	v_mov_b32_e32 v113, v0
	v_mov_b32_e32 v114, v0
	v_mov_b32_e32 v115, v0
	v_mov_b32_e32 v120, v0
	v_mov_b32_e32 v121, v0
	v_mov_b32_e32 v122, v0
	v_mov_b32_e32 v123, v0
	v_mov_b32_e32 v124, v0
	v_mov_b32_e32 v125, v0
	v_mov_b32_e32 v126, v0
	v_mov_b32_e32 v127, v0
; #define G_WAIT_L(n) asm volatile("s_waitcnt lgkmcnt(" #n ")" ::: "memory")
; #define G_BAR do { asm volatile("" ::: "memory"); __builtin_amdgcn_s_barrier(); asm volatile("" ::: "memory"); } while (0)
; #define G_SCHED __builtin_amdgcn_sched_barrier(0)
; #define STG_A(b, h, kt) do { const unsigned char* _g = A + (size_t)KT_(kt) * ASTEP; \
;         dma16((const void*)(_g + (size_t)((h) * 128) * ROWB), ROWB ? aoff[0][0] : aoff[h][0], lds_u + SA_(b, h) + dma0); \
;         dma16((const void*)(_g + (size_t)((h) * 128 + 64) * ROWB), ROWB ? aoff[0][0] : aoff[h][1], lds_u + SA_(b, h) + dma1); } while (0)
; #define STG_B(b, h, kt) do { const unsigned char* _g = img + (size_t)KT_(kt) * 32768 + (h) * 16384; \
;         dma16((const void*)(_g + dma0), boffl, lds_u + SB_(b, h) + dma0); \
;         dma16((const void*)(_g + dma1), boffl, lds_u + SB_(b, h) + dma1); } while (0)
; #define LDA_(dst, b, h) do { _Pragma("unroll") for (int _m = 0; _m < 4; ++_m) { \
;         dst[_m].lo = *(LAS3 const i32x4d*)(ap0 + SA_(b, h) + _m * 2048); \
;         dst[_m].hi = *(LAS3 const i32x4d*)(ap1 + SA_(b, h) + _m * 2048); } } while (0)
; #define LDBF(dst, b, h) do { _Pragma("unroll") for (int _n = 0; _n < 2; ++_n) { \
;         dst[_n].lo = *(LAS3 const i32x4d*)(bp0 + (SB_(b, h) - 4 * GHTB) + _n * 8192); \
;         dst[_n].hi = *(LAS3 const i32x4d*)(bp1 + (SB_(b, h) - 4 * GHTB) + _n * 8192); } } while (0)
;     ...
;         const int t1 = (t + 1 < nt) ? t + 1 : nt - 1, t2 = (t + 2 < nt) ? t + 2 : nt - 1, t3 = (t + 3 < nt) ? t + 3 : nt - 1;
;         LDBF(B0, 0, 0); G_SCHED; LDA_(At, 0, 0); STG_A(1, 1, t1);
;         G_WAIT_L(8); G_BAR; G_WAIT_L(0); MMAD(0, 0, At, B0); G_BAR; G_SCHED;
;         LDBF(B1, 0, 1); STG_B(0, 0, t2);
;         G_BAR; G_WAIT_L(0); MMAD(0, 1, At, B1); G_BAR;
;         LDA_(At, 0, 1); STG_A(0, 0, t2);
;         G_BAR; G_WAIT_L(0); MMAD(1, 0, At, B0); G_BAR; G_SCHED;
.LBB0_278:
	ds_read_b128 v[136:139], v132
	ds_read_b128 v[140:143], v132 offset:8192
	ds_read_b128 v[144:147], v133
	ds_read_b128 v[148:151], v133 offset:8192
	s_add_i32 s90, s26, 2
	s_add_i32 s26, s26, 4
	s_min_u32 s68, s26, 31
	ds_read_b128 v[152:155], v129
	ds_read_b128 v[156:159], v129 offset:2048
	ds_read_b128 v[160:163], v131
	ds_read_b128 v[164:167], v131 offset:2048
	ds_read_b128 v[168:171], v129 offset:4096
	ds_read_b128 v[172:175], v129 offset:6144
	ds_read_b128 v[176:179], v131 offset:4096
	ds_read_b128 v[180:183], v131 offset:6144
	s_add_u32 s26, s16, 0x80080
	s_addc_u32 s27, s17, 0
	s_mov_b32 m0, s71
	s_nop 0
	global_load_lds_dwordx4 v128, s[26:27]
	s_add_u32 s26, s16, 0xc0080
	s_addc_u32 s27, s17, 0
	s_mov_b32 m0, s86
	s_nop 0
	global_load_lds_dwordx4 v128, s[26:27]
	s_waitcnt lgkmcnt(8)
	s_waitcnt vmcnt(10)
	s_barrier
	s_waitcnt lgkmcnt(0)
	s_setprio 1
	s_waitcnt lgkmcnt(7)
	v_mfma_f32_16x16x32_bf16 v[124:127], v[136:139], v[152:155], v[124:127]
	v_mfma_f32_16x16x32_bf16 v[120:123], v[140:143], v[152:155], v[120:123]
	s_waitcnt lgkmcnt(6)
	v_mfma_f32_16x16x32_bf16 v[112:115], v[136:139], v[156:159], v[112:115]
	v_mfma_f32_16x16x32_bf16 v[108:111], v[140:143], v[156:159], v[108:111]
	s_waitcnt lgkmcnt(3)
	v_mfma_f32_16x16x32_bf16 v[96:99], v[136:139], v[168:171], v[96:99]
	v_mfma_f32_16x16x32_bf16 v[92:95], v[140:143], v[168:171], v[92:95]
	s_waitcnt lgkmcnt(2)
	v_mfma_f32_16x16x32_bf16 v[80:83], v[136:139], v[172:175], v[80:83]
	v_mfma_f32_16x16x32_bf16 v[76:79], v[140:143], v[172:175], v[76:79]
	v_mfma_f32_16x16x32_bf16 v[124:127], v[144:147], v[160:163], v[124:127]
	v_mfma_f32_16x16x32_bf16 v[120:123], v[148:151], v[160:163], v[120:123]
	v_mfma_f32_16x16x32_bf16 v[112:115], v[144:147], v[164:167], v[112:115]
	v_mfma_f32_16x16x32_bf16 v[108:111], v[148:151], v[164:167], v[108:111]
	s_waitcnt lgkmcnt(1)
	v_mfma_f32_16x16x32_bf16 v[96:99], v[144:147], v[176:179], v[96:99]
	v_mfma_f32_16x16x32_bf16 v[92:95], v[148:151], v[176:179], v[92:95]
	s_waitcnt lgkmcnt(0)
	v_mfma_f32_16x16x32_bf16 v[80:83], v[144:147], v[180:183], v[80:83]
	v_mfma_f32_16x16x32_bf16 v[76:79], v[148:151], v[180:183], v[76:79]
	s_setprio 0
	s_barrier
	s_lshl_b32 s26, s68, 15
	s_add_u32 s72, s88, s26
	s_addc_u32 s73, s89, 0
	s_add_u32 s26, s72, s20
	ds_read_b128 v[184:187], v132 offset:16384
	ds_read_b128 v[188:191], v132 offset:24576
	ds_read_b128 v[192:195], v133 offset:16384
	ds_read_b128 v[196:199], v133 offset:24576
	s_addc_u32 s27, s73, s22
	s_mov_b32 m0, s25
	s_nop 0
	global_load_lds_dwordx4 v134, s[26:27]
	s_add_u32 s26, s72, s21
	s_addc_u32 s27, s73, s28
	s_mov_b32 m0, s29
	s_nop 0
	global_load_lds_dwordx4 v134, s[26:27]
	s_waitcnt vmcnt(10)
	s_barrier
	s_waitcnt lgkmcnt(0)
	s_setprio 1
	s_waitcnt lgkmcnt(3)
	v_mfma_f32_16x16x32_bf16 v[116:119], v[184:187], v[152:155], v[116:119]
	s_waitcnt lgkmcnt(2)
	v_mfma_f32_16x16x32_bf16 v[104:107], v[188:191], v[152:155], v[104:107]
	v_mfma_f32_16x16x32_bf16 v[100:103], v[184:187], v[156:159], v[100:103]
	v_mfma_f32_16x16x32_bf16 v[88:91], v[188:191], v[156:159], v[88:91]
	v_mfma_f32_16x16x32_bf16 v[84:87], v[184:187], v[168:171], v[84:87]
	v_mfma_f32_16x16x32_bf16 v[72:75], v[188:191], v[168:171], v[72:75]
	v_mfma_f32_16x16x32_bf16 v[68:71], v[184:187], v[172:175], v[68:71]
	v_mfma_f32_16x16x32_bf16 v[64:67], v[188:191], v[172:175], v[64:67]
	s_waitcnt lgkmcnt(1)
	v_mfma_f32_16x16x32_bf16 v[116:119], v[192:195], v[160:163], v[116:119]
	s_waitcnt lgkmcnt(0)
	v_mfma_f32_16x16x32_bf16 v[104:107], v[196:199], v[160:163], v[104:107]
	v_mfma_f32_16x16x32_bf16 v[100:103], v[192:195], v[164:167], v[100:103]
	v_mfma_f32_16x16x32_bf16 v[88:91], v[196:199], v[164:167], v[88:91]
	v_mfma_f32_16x16x32_bf16 v[84:87], v[192:195], v[176:179], v[84:87]
	v_mfma_f32_16x16x32_bf16 v[72:75], v[196:199], v[176:179], v[72:75]
	v_mfma_f32_16x16x32_bf16 v[68:71], v[192:195], v[180:183], v[68:71]
	v_mfma_f32_16x16x32_bf16 v[64:67], v[196:199], v[180:183], v[64:67]
	s_setprio 0
	s_barrier
	ds_read_b128 v[152:155], v129 offset:16384
	ds_read_b128 v[156:159], v129 offset:18432
	ds_read_b128 v[160:163], v131 offset:16384
	ds_read_b128 v[164:167], v131 offset:18432
	ds_read_b128 v[168:171], v129 offset:20480
	ds_read_b128 v[172:175], v129 offset:22528
	ds_read_b128 v[176:179], v131 offset:20480
	ds_read_b128 v[180:183], v131 offset:22528
	s_lshl_b32 s26, s68, 7
	s_add_u32 s26, s60, s26
	s_addc_u32 s27, s61, 0
	s_mov_b32 m0, s23
	s_nop 0
	global_load_lds_dwordx4 v128, s[26:27]
	s_add_u32 s68, s26, 0x40000
	s_addc_u32 s69, s27, 0
	s_mov_b32 m0, s30
	s_nop 0
	global_load_lds_dwordx4 v128, s[68:69]
	s_barrier
	s_waitcnt lgkmcnt(0)
	s_setprio 1
	s_waitcnt lgkmcnt(7)
	v_mfma_f32_16x16x32_bf16 v[60:63], v[136:139], v[152:155], v[60:63]
	v_mfma_f32_16x16x32_bf16 v[56:59], v[140:143], v[152:155], v[56:59]
	s_waitcnt lgkmcnt(6)
	v_mfma_f32_16x16x32_bf16 v[48:51], v[136:139], v[156:159], v[48:51]
	v_mfma_f32_16x16x32_bf16 v[44:47], v[140:143], v[156:159], v[44:47]
	s_waitcnt lgkmcnt(3)
	v_mfma_f32_16x16x32_bf16 v[32:35], v[136:139], v[168:171], v[32:35]
	v_mfma_f32_16x16x32_bf16 v[28:31], v[140:143], v[168:171], v[28:31]
	s_waitcnt lgkmcnt(2)
	v_mfma_f32_16x16x32_bf16 v[16:19], v[136:139], v[172:175], v[16:19]
	v_mfma_f32_16x16x32_bf16 v[12:15], v[140:143], v[172:175], v[12:15]
	v_mfma_f32_16x16x32_bf16 v[60:63], v[144:147], v[160:163], v[60:63]
	v_mfma_f32_16x16x32_bf16 v[56:59], v[148:151], v[160:163], v[56:59]
	v_mfma_f32_16x16x32_bf16 v[48:51], v[144:147], v[164:167], v[48:51]
	v_mfma_f32_16x16x32_bf16 v[44:47], v[148:151], v[164:167], v[44:47]
	s_waitcnt lgkmcnt(1)
	v_mfma_f32_16x16x32_bf16 v[32:35], v[144:147], v[176:179], v[32:35]
	v_mfma_f32_16x16x32_bf16 v[28:31], v[148:151], v[176:179], v[28:31]
	s_waitcnt lgkmcnt(0)
	v_mfma_f32_16x16x32_bf16 v[16:19], v[144:147], v[180:183], v[16:19]
	v_mfma_f32_16x16x32_bf16 v[12:15], v[148:151], v[180:183], v[12:15]
	s_setprio 0
	s_barrier
; #define G_WAIT_V(n) asm volatile("s_waitcnt vmcnt(" #n ")" ::: "memory")
; #define G_WAIT_L(n) asm volatile("s_waitcnt lgkmcnt(" #n ")" ::: "memory")
; #define G_BAR do { asm volatile("" ::: "memory"); __builtin_amdgcn_s_barrier(); asm volatile("" ::: "memory"); } while (0)
; #define G_SCHED __builtin_amdgcn_sched_barrier(0)
; #define STG_A(b, h, kt) do { const unsigned char* _g = A + (size_t)KT_(kt) * ASTEP; \
;         dma16((const void*)(_g + (size_t)((h) * 128) * ROWB), ROWB ? aoff[0][0] : aoff[h][0], lds_u + SA_(b, h) + dma0); \
;         dma16((const void*)(_g + (size_t)((h) * 128 + 64) * ROWB), ROWB ? aoff[0][0] : aoff[h][1], lds_u + SA_(b, h) + dma1); } while (0)
; #define STG_B(b, h, kt) do { const unsigned char* _g = img + (size_t)KT_(kt) * 32768 + (h) * 16384; \
;         dma16((const void*)(_g + dma0), boffl, lds_u + SB_(b, h) + dma0); \
;         dma16((const void*)(_g + dma1), boffl, lds_u + SB_(b, h) + dma1); } while (0)
; #define LDA_(dst, b, h) do { _Pragma("unroll") for (int _m = 0; _m < 4; ++_m) { \
;         dst[_m].lo = *(LAS3 const i32x4d*)(ap0 + SA_(b, h) + _m * 2048); \
;         dst[_m].hi = *(LAS3 const i32x4d*)(ap1 + SA_(b, h) + _m * 2048); } } while (0)
; #define LDBF(dst, b, h) do { _Pragma("unroll") for (int _n = 0; _n < 2; ++_n) { \
;         dst[_n].lo = *(LAS3 const i32x4d*)(bp0 + (SB_(b, h) - 4 * GHTB) + _n * 8192); \
;         dst[_n].hi = *(LAS3 const i32x4d*)(bp1 + (SB_(b, h) - 4 * GHTB) + _n * 8192); } } while (0)
;     ...
;         STG_B(0, 1, t2);
;         G_WAIT_V(6); G_BAR; MMAD(1, 1, At, B1); G_BAR;
;         LDBF(B0, 1, 0); G_SCHED; LDA_(At, 1, 0); STG_A(0, 1, t2);
;         G_WAIT_L(8); G_BAR; G_WAIT_L(0); MMAD(0, 0, At, B0); G_BAR; G_SCHED;
;         LDBF(B1, 1, 1); STG_B(1, 0, t3);
	s_add_u32 s72, s72, 0x4000
	s_addc_u32 s73, s73, 0
	s_add_u32 s68, s72, s20
	s_addc_u32 s69, s73, s22
	s_mov_b32 m0, s31
	s_nop 0
	global_load_lds_dwordx4 v134, s[68:69]
	s_add_u32 s68, s72, s21
	s_addc_u32 s69, s73, s28
	s_mov_b32 m0, s33
	s_nop 0
	global_load_lds_dwordx4 v134, s[68:69]
	s_waitcnt vmcnt(10)
	s_barrier
	s_setprio 1
	v_mfma_f32_16x16x32_bf16 v[52:55], v[184:187], v[152:155], v[52:55]
	v_mfma_f32_16x16x32_bf16 v[40:43], v[188:191], v[152:155], v[40:43]
	v_mfma_f32_16x16x32_bf16 v[36:39], v[184:187], v[156:159], v[36:39]
	v_mfma_f32_16x16x32_bf16 v[24:27], v[188:191], v[156:159], v[24:27]
	v_mfma_f32_16x16x32_bf16 v[20:23], v[184:187], v[168:171], v[20:23]
	v_mfma_f32_16x16x32_bf16 v[8:11], v[188:191], v[168:171], v[8:11]
	v_mfma_f32_16x16x32_bf16 v[4:7], v[184:187], v[172:175], v[4:7]
	v_mfma_f32_16x16x32_bf16 v[0:3], v[188:191], v[172:175], v[0:3]
	v_mfma_f32_16x16x32_bf16 v[52:55], v[192:195], v[160:163], v[52:55]
	v_mfma_f32_16x16x32_bf16 v[40:43], v[196:199], v[160:163], v[40:43]
	v_mfma_f32_16x16x32_bf16 v[36:39], v[192:195], v[164:167], v[36:39]
	v_mfma_f32_16x16x32_bf16 v[24:27], v[196:199], v[164:167], v[24:27]
	v_mfma_f32_16x16x32_bf16 v[20:23], v[192:195], v[176:179], v[20:23]
	v_mfma_f32_16x16x32_bf16 v[8:11], v[196:199], v[176:179], v[8:11]
	v_mfma_f32_16x16x32_bf16 v[4:7], v[192:195], v[180:183], v[4:7]
	v_mfma_f32_16x16x32_bf16 v[0:3], v[196:199], v[180:183], v[0:3]
	s_setprio 0
	s_barrier
	ds_read_b128 v[136:139], v132 offset:32768
	ds_read_b128 v[140:143], v132 offset:40960
	ds_read_b128 v[144:147], v133 offset:32768
	ds_read_b128 v[148:151], v133 offset:40960
	ds_read_b128 v[152:155], v129 offset:32768
	ds_read_b128 v[156:159], v129 offset:34816
	ds_read_b128 v[160:163], v131 offset:32768
	ds_read_b128 v[164:167], v131 offset:34816
	ds_read_b128 v[168:171], v129 offset:36864
	ds_read_b128 v[172:175], v129 offset:38912
	ds_read_b128 v[176:179], v131 offset:36864
	ds_read_b128 v[180:183], v131 offset:38912
	s_add_u32 s68, s26, 0x80000
	s_addc_u32 s69, s27, 0
	s_mov_b32 m0, s34
	s_nop 0
	global_load_lds_dwordx4 v128, s[68:69]
	s_add_u32 s26, s26, 0xc0000
	s_addc_u32 s27, s27, 0
	s_mov_b32 m0, s54
	s_nop 0
	global_load_lds_dwordx4 v128, s[26:27]
	s_waitcnt lgkmcnt(8)
	s_waitcnt vmcnt(10)
	s_barrier
	s_waitcnt lgkmcnt(0)
	s_setprio 1
	s_waitcnt lgkmcnt(7)
	v_mfma_f32_16x16x32_bf16 v[124:127], v[136:139], v[152:155], v[124:127]
	v_mfma_f32_16x16x32_bf16 v[120:123], v[140:143], v[152:155], v[120:123]
	s_waitcnt lgkmcnt(6)
	v_mfma_f32_16x16x32_bf16 v[112:115], v[136:139], v[156:159], v[112:115]
	v_mfma_f32_16x16x32_bf16 v[108:111], v[140:143], v[156:159], v[108:111]
	s_waitcnt lgkmcnt(3)
	v_mfma_f32_16x16x32_bf16 v[96:99], v[136:139], v[168:171], v[96:99]
	v_mfma_f32_16x16x32_bf16 v[92:95], v[140:143], v[168:171], v[92:95]
	s_waitcnt lgkmcnt(2)
	v_mfma_f32_16x16x32_bf16 v[80:83], v[136:139], v[172:175], v[80:83]
	v_mfma_f32_16x16x32_bf16 v[76:79], v[140:143], v[172:175], v[76:79]
	v_mfma_f32_16x16x32_bf16 v[124:127], v[144:147], v[160:163], v[124:127]
	v_mfma_f32_16x16x32_bf16 v[120:123], v[148:151], v[160:163], v[120:123]
	v_mfma_f32_16x16x32_bf16 v[112:115], v[144:147], v[164:167], v[112:115]
	v_mfma_f32_16x16x32_bf16 v[108:111], v[148:151], v[164:167], v[108:111]
	s_waitcnt lgkmcnt(1)
	v_mfma_f32_16x16x32_bf16 v[96:99], v[144:147], v[176:179], v[96:99]
	v_mfma_f32_16x16x32_bf16 v[92:95], v[148:151], v[176:179], v[92:95]
	s_waitcnt lgkmcnt(0)
	v_mfma_f32_16x16x32_bf16 v[80:83], v[144:147], v[180:183], v[80:83]
	v_mfma_f32_16x16x32_bf16 v[76:79], v[148:151], v[180:183], v[76:79]
	s_setprio 0
	s_barrier
	s_min_u32 s26, s90, 28
	s_add_i32 s68, s26, 3
	s_lshl_b32 s26, s68, 15
	s_add_u32 s69, s88, s26
	s_addc_u32 s72, s89, 0
	s_add_u32 s26, s69, s20
	ds_read_b128 v[184:187], v132 offset:49152
	ds_read_b128 v[188:191], v132 offset:57344
	ds_read_b128 v[192:195], v133 offset:49152
	ds_read_b128 v[196:199], v133 offset:57344
	s_addc_u32 s27, s72, s22
	s_mov_b32 m0, s55
	s_nop 0
	global_load_lds_dwordx4 v134, s[26:27]
	s_add_u32 s26, s69, s21
	s_addc_u32 s27, s72, s28
	s_mov_b32 m0, s56
	s_nop 0
	global_load_lds_dwordx4 v134, s[26:27]
	s_waitcnt vmcnt(10)
	s_barrier
; #define G_WAIT_V(n) asm volatile("s_waitcnt vmcnt(" #n ")" ::: "memory")
; #define G_WAIT_L(n) asm volatile("s_waitcnt lgkmcnt(" #n ")" ::: "memory")
; #define G_BAR do { asm volatile("" ::: "memory"); __builtin_amdgcn_s_barrier(); asm volatile("" ::: "memory"); } while (0)
; #define G_SCHED __builtin_amdgcn_sched_barrier(0)
; #define STG_A(b, h, kt) do { const unsigned char* _g = A + (size_t)KT_(kt) * ASTEP; \
;         dma16((const void*)(_g + (size_t)((h) * 128) * ROWB), ROWB ? aoff[0][0] : aoff[h][0], lds_u + SA_(b, h) + dma0); \
;         dma16((const void*)(_g + (size_t)((h) * 128 + 64) * ROWB), ROWB ? aoff[0][0] : aoff[h][1], lds_u + SA_(b, h) + dma1); } while (0)
; #define STG_B(b, h, kt) do { const unsigned char* _g = img + (size_t)KT_(kt) * 32768 + (h) * 16384; \
;         dma16((const void*)(_g + dma0), boffl, lds_u + SB_(b, h) + dma0); \
;         dma16((const void*)(_g + dma1), boffl, lds_u + SB_(b, h) + dma1); } while (0)
; #define LDA_(dst, b, h) do { _Pragma("unroll") for (int _m = 0; _m < 4; ++_m) { \
;         dst[_m].lo = *(LAS3 const i32x4d*)(ap0 + SA_(b, h) + _m * 2048); \
;         dst[_m].hi = *(LAS3 const i32x4d*)(ap1 + SA_(b, h) + _m * 2048); } } while (0)
;     ...
;         G_BAR; G_WAIT_L(0); MMAD(0, 1, At, B1); G_BAR;
;         LDA_(At, 1, 1); STG_A(1, 0, t3);
;         G_BAR; G_WAIT_L(0); MMAD(1, 0, At, B0); G_BAR; G_SCHED;
;         STG_B(1, 1, t3);
;         G_WAIT_V(6); G_BAR; MMAD(1, 1, At, B1); G_BAR;
;     }
;     G_WAIT_V(0); G_WAIT_L(0);
;     { int wr0 = wid >> 2; asm volatile("" : "+s"(wr0)); if (wr0 == 0) G_BAR; }
;     G_BAR;
	s_waitcnt lgkmcnt(0)
	s_setprio 1
	s_waitcnt lgkmcnt(3)
	v_mfma_f32_16x16x32_bf16 v[116:119], v[184:187], v[152:155], v[116:119]
	s_waitcnt lgkmcnt(2)
	v_mfma_f32_16x16x32_bf16 v[104:107], v[188:191], v[152:155], v[104:107]
	v_mfma_f32_16x16x32_bf16 v[100:103], v[184:187], v[156:159], v[100:103]
	v_mfma_f32_16x16x32_bf16 v[88:91], v[188:191], v[156:159], v[88:91]
	v_mfma_f32_16x16x32_bf16 v[84:87], v[184:187], v[168:171], v[84:87]
	v_mfma_f32_16x16x32_bf16 v[72:75], v[188:191], v[168:171], v[72:75]
	v_mfma_f32_16x16x32_bf16 v[68:71], v[184:187], v[172:175], v[68:71]
	v_mfma_f32_16x16x32_bf16 v[64:67], v[188:191], v[172:175], v[64:67]
	s_waitcnt lgkmcnt(1)
	v_mfma_f32_16x16x32_bf16 v[116:119], v[192:195], v[160:163], v[116:119]
	s_waitcnt lgkmcnt(0)
	v_mfma_f32_16x16x32_bf16 v[104:107], v[196:199], v[160:163], v[104:107]
	v_mfma_f32_16x16x32_bf16 v[100:103], v[192:195], v[164:167], v[100:103]
	v_mfma_f32_16x16x32_bf16 v[88:91], v[196:199], v[164:167], v[88:91]
	v_mfma_f32_16x16x32_bf16 v[84:87], v[192:195], v[176:179], v[84:87]
	v_mfma_f32_16x16x32_bf16 v[72:75], v[196:199], v[176:179], v[72:75]
	v_mfma_f32_16x16x32_bf16 v[68:71], v[192:195], v[180:183], v[68:71]
	v_mfma_f32_16x16x32_bf16 v[64:67], v[196:199], v[180:183], v[64:67]
	s_setprio 0
	s_barrier
	ds_read_b128 v[152:155], v129 offset:49152
	ds_read_b128 v[156:159], v129 offset:51200
	ds_read_b128 v[160:163], v131 offset:49152
	ds_read_b128 v[164:167], v131 offset:51200
	ds_read_b128 v[168:171], v129 offset:53248
	ds_read_b128 v[172:175], v129 offset:55296
	ds_read_b128 v[176:179], v131 offset:53248
	ds_read_b128 v[180:183], v131 offset:55296
	s_lshl_b32 s26, s68, 7
	s_add_u32 s26, s60, s26
	s_addc_u32 s27, s61, 0
	s_mov_b32 m0, s57
	s_nop 0
	global_load_lds_dwordx4 v128, s[26:27]
	s_add_u32 s26, s26, 0x40000
	s_addc_u32 s27, s27, 0
	s_mov_b32 m0, s58
	s_nop 0
	global_load_lds_dwordx4 v128, s[26:27]
	s_barrier
	s_waitcnt lgkmcnt(0)
	s_setprio 1
	s_waitcnt lgkmcnt(7)
	v_mfma_f32_16x16x32_bf16 v[60:63], v[136:139], v[152:155], v[60:63]
	v_mfma_f32_16x16x32_bf16 v[56:59], v[140:143], v[152:155], v[56:59]
	s_waitcnt lgkmcnt(6)
	v_mfma_f32_16x16x32_bf16 v[48:51], v[136:139], v[156:159], v[48:51]
	v_mfma_f32_16x16x32_bf16 v[44:47], v[140:143], v[156:159], v[44:47]
	s_waitcnt lgkmcnt(3)
	v_mfma_f32_16x16x32_bf16 v[32:35], v[136:139], v[168:171], v[32:35]
	v_mfma_f32_16x16x32_bf16 v[28:31], v[140:143], v[168:171], v[28:31]
	s_waitcnt lgkmcnt(2)
	v_mfma_f32_16x16x32_bf16 v[16:19], v[136:139], v[172:175], v[16:19]
	v_mfma_f32_16x16x32_bf16 v[12:15], v[140:143], v[172:175], v[12:15]
	v_mfma_f32_16x16x32_bf16 v[60:63], v[144:147], v[160:163], v[60:63]
	v_mfma_f32_16x16x32_bf16 v[56:59], v[148:151], v[160:163], v[56:59]
	v_mfma_f32_16x16x32_bf16 v[48:51], v[144:147], v[164:167], v[48:51]
	v_mfma_f32_16x16x32_bf16 v[44:47], v[148:151], v[164:167], v[44:47]
	s_waitcnt lgkmcnt(1)
	v_mfma_f32_16x16x32_bf16 v[32:35], v[144:147], v[176:179], v[32:35]
	v_mfma_f32_16x16x32_bf16 v[28:31], v[148:151], v[176:179], v[28:31]
	s_waitcnt lgkmcnt(0)
	v_mfma_f32_16x16x32_bf16 v[16:19], v[144:147], v[180:183], v[16:19]
	v_mfma_f32_16x16x32_bf16 v[12:15], v[148:151], v[180:183], v[12:15]
	s_setprio 0
	s_barrier
	s_add_u32 s68, s69, 0x4000
	s_addc_u32 s69, s72, 0
	s_add_u32 s26, s68, s20
	s_addc_u32 s27, s69, s22
	s_mov_b32 m0, s59
	s_nop 0
	global_load_lds_dwordx4 v134, s[26:27]
	s_add_u32 s26, s68, s21
	s_addc_u32 s27, s69, s28
	s_mov_b32 m0, s70
	s_nop 0
	global_load_lds_dwordx4 v134, s[26:27]
	s_waitcnt vmcnt(10)
	s_barrier
	s_setprio 1
	v_mfma_f32_16x16x32_bf16 v[52:55], v[184:187], v[152:155], v[52:55]
	v_mfma_f32_16x16x32_bf16 v[40:43], v[188:191], v[152:155], v[40:43]
	v_mfma_f32_16x16x32_bf16 v[36:39], v[184:187], v[156:159], v[36:39]
	v_mfma_f32_16x16x32_bf16 v[24:27], v[188:191], v[156:159], v[24:27]
	v_mfma_f32_16x16x32_bf16 v[20:23], v[184:187], v[168:171], v[20:23]
	v_mfma_f32_16x16x32_bf16 v[8:11], v[188:191], v[168:171], v[8:11]
	v_mfma_f32_16x16x32_bf16 v[4:7], v[184:187], v[172:175], v[4:7]
	v_mfma_f32_16x16x32_bf16 v[0:3], v[188:191], v[172:175], v[0:3]
	v_mfma_f32_16x16x32_bf16 v[52:55], v[192:195], v[160:163], v[52:55]
	v_mfma_f32_16x16x32_bf16 v[40:43], v[196:199], v[160:163], v[40:43]
	v_mfma_f32_16x16x32_bf16 v[36:39], v[192:195], v[164:167], v[36:39]
	v_mfma_f32_16x16x32_bf16 v[24:27], v[196:199], v[164:167], v[24:27]
	v_mfma_f32_16x16x32_bf16 v[20:23], v[192:195], v[176:179], v[20:23]
	v_mfma_f32_16x16x32_bf16 v[8:11], v[196:199], v[176:179], v[8:11]
	v_mfma_f32_16x16x32_bf16 v[4:7], v[192:195], v[180:183], v[4:7]
	v_mfma_f32_16x16x32_bf16 v[0:3], v[196:199], v[180:183], v[0:3]
	s_setprio 0
	s_barrier
	s_add_u32 s16, s16, 0x100
	s_addc_u32 s17, s17, 0
	s_cmp_gt_u32 s90, 29
	s_mov_b32 s26, s90
	s_cbranch_scc0 .LBB0_278
	s_waitcnt vmcnt(0)
	s_waitcnt lgkmcnt(0)
	s_mov_b32 s16, s3
	s_cmp_eq_u32 s16, 0
	s_cbranch_scc0 .LBB0_274
	s_barrier
	s_branch .LBB0_274

; #define G_BAR do { asm volatile("" ::: "memory"); __builtin_amdgcn_s_barrier(); asm volatile("" ::: "memory"); } while (0)
; #define STG_A(b, h, kt) do { const unsigned char* _g = A + (size_t)KT_(kt) * ASTEP; \
;         dma16((const void*)(_g + (size_t)((h) * 128) * ROWB), ROWB ? aoff[0][0] : aoff[h][0], lds_u + SA_(b, h) + dma0); \
;         dma16((const void*)(_g + (size_t)((h) * 128 + 64) * ROWB), ROWB ? aoff[0][0] : aoff[h][1], lds_u + SA_(b, h) + dma1); } while (0)
; #define STG_B(b, h, kt) do { const unsigned char* _g = img + (size_t)KT_(kt) * 32768 + (h) * 16384; \
;         dma16((const void*)(_g + dma0), boffl, lds_u + SB_(b, h) + dma0); \
;         dma16((const void*)(_g + dma1), boffl, lds_u + SB_(b, h) + dma1); } while (0)
;     ...
;     STG_B(0, 0, 0); STG_A(0, 0, 0); STG_B(0, 1, 0); STG_A(0, 1, 0);
;     __builtin_amdgcn_s_waitcnt(0);
;     { int wr1 = wid >> 2; asm volatile("" : "+s"(wr1)); if (wr1 == 1) G_BAR; }
;     G_BAR;
; template <int EPI>
; __device__ __forceinline__ void gemm_tile_img(const GemmArgs& g, int pm, int pn, int e, int ebase, int ecnt, LAS3 char* lds, int wid, const unsigned char* img, const TileSync& sy, int kh = -1) {
;     ...
;     for (int h = 0; h < 2; ++h)
; #pragma unroll
;         for (int i = 0; i < 2; ++i) {
;             const int rih = (i * 8 + wid) * 8 + (lane >> 3);
;             const int chunk = (lane & 7) ^ ((rih >> 1) & 7);
;             int r = pm * 256 + h * 128 + rih;
;             unsigned grow;
;             if (EPI == 2) { if (r >= ecnt) r = ecnt - 1; grow = (unsigned)(g.list[e * T + r] >> 2); }
;             else if (EPI == 3) { grow = (unsigned)(((g.abase >> 8) + pm) * (16 * 256) + h * 128 + rih); }
;             else grow = (unsigned)r;
;             aoff[h][i] = (EPI == 3) ? (grow * 128u + (unsigned)(chunk * 16)) : (EPI >= 2) ? (grow * (unsigned)D + (unsigned)(chunk * 16)) : (grow * (unsigned)D + (unsigned)(chunk * 8)) * 2u;
;         }
.LBB0_467:
	s_or_b64 exec, exec, s[0:1]
	v_lshrrev_b32_e32 v1, 1, v2
	v_xor_b32_e32 v1, v1, v0
	v_lshlrev_b32_e32 v1, 4, v1
	s_waitcnt vmcnt(3)
	v_lshlrev_b32_e32 v2, 9, v3
	v_and_b32_e32 v1, 0x70, v1
	s_movk_i32 s0, 0xf800
	v_and_or_b32 v144, v2, s0, v1
	s_waitcnt vmcnt(2)
	v_lshlrev_b32_e32 v2, 9, v4
	v_and_or_b32 v152, v2, s0, v1
	s_waitcnt vmcnt(1)
	v_lshlrev_b32_e32 v2, 9, v5
	v_and_or_b32 v153, v2, s0, v1
	s_waitcnt vmcnt(0)
	v_lshlrev_b32_e32 v2, 9, v6
	s_or_b32 s4, s4, s24
	v_readlane_b32 s36, v254, 20
	v_and_or_b32 v154, v2, s0, v1
	s_lshl_b64 s[0:1], s[4:5], 19
	v_readlane_b32 s42, v254, 26
	s_add_u32 s4, s42, s0
	v_and_b32_e32 v1, 63, v0
	v_lshlrev_b32_e32 v3, 3, v0
	s_movk_i32 s0, 0x70
	v_and_b32_e32 v2, 15, v0
	v_bitop3_b32 v0, v3, v0, 63 bitop3:0x78
	v_bitop3_b32 v3, v3, s0, v1 bitop3:0x48
	v_readlane_b32 s0, v254, 60
	v_readlane_b32 s43, v254, 27
	s_addc_u32 vcc_lo, s43, s1
	v_or_b32_e32 v4, s0, v2
	v_readlane_b32 s0, v254, 61
	v_bitop3_b32 v0, v0, 64, v156 bitop3:0x6c
	s_waitcnt lgkmcnt(0)
	v_lshl_add_u32 v2, v2, 7, s0
	s_add_i32 s0, 0, 0x10000
	v_add_u32_e32 v155, v2, v3
	v_add_u32_e32 v156, v2, v0
	v_lshl_add_u32 v2, v4, 7, s0
	s_add_u32 s0, s4, s91
	v_add_u32_e32 v157, v2, v3
	v_add_u32_e32 v158, v2, v0
	s_addc_u32 s1, vcc_lo, s93
	s_barrier
	v_lshlrev_b32_e32 v159, 4, v1
	s_mov_b32 m0, s78
	s_nop 0
	global_load_lds_dwordx4 v159, s[0:1]
	s_add_u32 s0, s4, s92
	s_addc_u32 s1, vcc_lo, s96
	s_mov_b32 m0, s69
	s_nop 0
	global_load_lds_dwordx4 v159, s[0:1]
	s_mov_b32 m0, s94
	s_nop 0
	global_load_lds_dwordx4 v144, s[62:63]
	s_add_u32 s25, s4, 0x4000
	s_mov_b32 m0, s72
	s_nop 0
	global_load_lds_dwordx4 v152, s[62:63]
	s_addc_u32 s28, vcc_lo, 0
	s_add_u32 s0, s25, s91
	s_addc_u32 s1, s28, s93
	s_mov_b32 m0, s70
	s_nop 0
	global_load_lds_dwordx4 v159, s[0:1]
	s_add_u32 s0, s25, s92
	s_addc_u32 s1, s28, s96
	s_mov_b32 m0, s71
	s_nop 0
	global_load_lds_dwordx4 v159, s[0:1]
	s_mov_b32 m0, s61
	s_nop 0
	global_load_lds_dwordx4 v153, s[62:63]
	v_writelane_b32 v255, s74, 24
	s_mov_b32 m0, s59
	s_nop 0
	global_load_lds_dwordx4 v154, s[62:63]
	s_mov_b32 s0, s77
	v_writelane_b32 v255, s73, 25
	v_mov_b32_e32 v145, 0x70
	v_mov_b32_e32 v16, 0
	v_mov_b32_e32 v17, v16
	v_mov_b32_e32 v18, v16
	v_mov_b32_e32 v19, v16
	v_mov_b32_e32 v24, v16
	v_mov_b32_e32 v25, v16
	v_mov_b32_e32 v26, v16
	v_mov_b32_e32 v27, v16
	v_mov_b32_e32 v32, v16
	v_mov_b32_e32 v33, v16
	v_mov_b32_e32 v34, v16
	v_mov_b32_e32 v35, v16
	v_mov_b32_e32 v40, v16
	v_mov_b32_e32 v41, v16
	v_mov_b32_e32 v42, v16
	v_mov_b32_e32 v43, v16
	v_mov_b32_e32 v48, v16
	v_mov_b32_e32 v49, v16
	v_mov_b32_e32 v50, v16
	v_mov_b32_e32 v51, v16
	v_mov_b32_e32 v56, v16
	v_mov_b32_e32 v57, v16
	v_mov_b32_e32 v58, v16
	v_mov_b32_e32 v59, v16
	v_mov_b32_e32 v64, v16
	v_mov_b32_e32 v65, v16
	v_mov_b32_e32 v66, v16
	v_mov_b32_e32 v67, v16
	v_mov_b32_e32 v72, v16
	v_mov_b32_e32 v73, v16
	v_mov_b32_e32 v74, v16
	v_mov_b32_e32 v75, v16
	v_mov_b32_e32 v240, v16
	v_mov_b32_e32 v241, v16
	v_mov_b32_e32 v242, v16
	v_mov_b32_e32 v243, v16
	v_mov_b32_e32 v28, v16
	v_mov_b32_e32 v29, v16
	v_mov_b32_e32 v30, v16
	v_mov_b32_e32 v31, v16
	v_mov_b32_e32 v36, v16
	v_mov_b32_e32 v37, v16
	v_mov_b32_e32 v38, v16
	v_mov_b32_e32 v39, v16
	v_mov_b32_e32 v44, v16
	v_mov_b32_e32 v45, v16
	v_mov_b32_e32 v46, v16
	v_mov_b32_e32 v47, v16
	v_mov_b32_e32 v52, v16
	v_mov_b32_e32 v53, v16
	v_mov_b32_e32 v54, v16
	v_mov_b32_e32 v55, v16
	v_mov_b32_e32 v60, v16
	v_mov_b32_e32 v61, v16
	v_mov_b32_e32 v62, v16
	v_mov_b32_e32 v63, v16
	v_mov_b32_e32 v68, v16
	v_mov_b32_e32 v69, v16
	v_mov_b32_e32 v70, v16
	v_mov_b32_e32 v71, v16
	v_mov_b32_e32 v76, v16
	v_mov_b32_e32 v77, v16
	v_mov_b32_e32 v78, v16
	v_mov_b32_e32 v79, v16
	v_mov_b32_e32 v20, v16
	v_mov_b32_e32 v21, v16
	v_mov_b32_e32 v22, v16
	v_mov_b32_e32 v23, v16
	v_mov_b32_e32 v88, v16
	v_mov_b32_e32 v89, v16
	v_mov_b32_e32 v90, v16
	v_mov_b32_e32 v91, v16
	v_mov_b32_e32 v96, v16
	v_mov_b32_e32 v97, v16
	v_mov_b32_e32 v98, v16
	v_mov_b32_e32 v99, v16
	v_mov_b32_e32 v104, v16
	v_mov_b32_e32 v105, v16
	v_mov_b32_e32 v106, v16
	v_mov_b32_e32 v107, v16
	v_mov_b32_e32 v112, v16
	v_mov_b32_e32 v113, v16
	v_mov_b32_e32 v114, v16
	v_mov_b32_e32 v115, v16
	v_mov_b32_e32 v120, v16
	v_mov_b32_e32 v121, v16
	v_mov_b32_e32 v122, v16
	v_mov_b32_e32 v123, v16
	v_mov_b32_e32 v128, v16
	v_mov_b32_e32 v129, v16
	v_mov_b32_e32 v130, v16
	v_mov_b32_e32 v131, v16
	v_mov_b32_e32 v136, v16
	v_mov_b32_e32 v137, v16
	v_mov_b32_e32 v138, v16
	v_mov_b32_e32 v139, v16
	v_mov_b32_e32 v84, v16
	v_mov_b32_e32 v85, v16
	v_mov_b32_e32 v86, v16
	v_mov_b32_e32 v87, v16
	v_mov_b32_e32 v92, v16
	v_mov_b32_e32 v93, v16
	v_mov_b32_e32 v94, v16
	v_mov_b32_e32 v95, v16
	v_mov_b32_e32 v100, v16
	v_mov_b32_e32 v101, v16
	v_mov_b32_e32 v102, v16
	v_mov_b32_e32 v103, v16
	v_mov_b32_e32 v108, v16
	v_mov_b32_e32 v109, v16
	v_mov_b32_e32 v110, v16
	v_mov_b32_e32 v111, v16
	v_mov_b32_e32 v116, v16
	v_mov_b32_e32 v117, v16
	v_mov_b32_e32 v118, v16
	v_mov_b32_e32 v119, v16
	v_mov_b32_e32 v124, v16
	v_mov_b32_e32 v125, v16
	v_mov_b32_e32 v126, v16
	v_mov_b32_e32 v127, v16
	v_mov_b32_e32 v132, v16
	v_mov_b32_e32 v133, v16
	v_mov_b32_e32 v134, v16
	v_mov_b32_e32 v135, v16
	v_mov_b32_e32 v140, v16
	v_mov_b32_e32 v141, v16
	v_mov_b32_e32 v142, v16
	v_mov_b32_e32 v143, v16
	s_waitcnt vmcnt(0) expcnt(0) lgkmcnt(0)
	s_cmp_lg_u32 s0, 1
	v_readlane_b32 s37, v254, 21
	v_readlane_b32 s38, v254, 22
	v_readlane_b32 s39, v254, 23
	v_readlane_b32 s40, v254, 24
	v_readlane_b32 s41, v254, 25
	v_readlane_b32 s44, v254, 28
	v_readlane_b32 s45, v254, 29
	v_readlane_b32 s46, v254, 30
	v_readlane_b32 s47, v254, 31
	v_readlane_b32 s48, v254, 32
	v_readlane_b32 s49, v254, 33
	v_readlane_b32 s50, v254, 34
	v_readlane_b32 s51, v254, 35
	s_cbranch_scc1 .LBB0_469
	s_barrier
; #define G_WAIT_V(n) asm volatile("s_waitcnt vmcnt(" #n ")" ::: "memory")
; #define G_WAIT_L(n) asm volatile("s_waitcnt lgkmcnt(" #n ")" ::: "memory")
; #define G_BAR do { asm volatile("" ::: "memory"); __builtin_amdgcn_s_barrier(); asm volatile("" ::: "memory"); } while (0)
; #define G_SCHED __builtin_amdgcn_sched_barrier(0)
; #define STG_A(b, h, kt) do { const unsigned char* _g = A + (size_t)KT_(kt) * ASTEP; \
;         dma16((const void*)(_g + (size_t)((h) * 128) * ROWB), ROWB ? aoff[0][0] : aoff[h][0], lds_u + SA_(b, h) + dma0); \
;         dma16((const void*)(_g + (size_t)((h) * 128 + 64) * ROWB), ROWB ? aoff[0][0] : aoff[h][1], lds_u + SA_(b, h) + dma1); } while (0)
; #define STG_B(b, h, kt) do { const unsigned char* _g = img + (size_t)KT_(kt) * 32768 + (h) * 16384; \
;         dma16((const void*)(_g + dma0), boffl, lds_u + SB_(b, h) + dma0); \
;         dma16((const void*)(_g + dma1), boffl, lds_u + SB_(b, h) + dma1); } while (0)
; #define LDA_(dst, b, h) do { _Pragma("unroll") for (int _m = 0; _m < 4; ++_m) { \
;         dst[_m].lo = *(LAS3 const i32x4d*)(ap0 + SA_(b, h) + _m * 2048); \
;         dst[_m].hi = *(LAS3 const i32x4d*)(ap1 + SA_(b, h) + _m * 2048); } } while (0)
; #define LDBF(dst, b, h) do { _Pragma("unroll") for (int _n = 0; _n < 2; ++_n) { \
;         dst[_n].lo = *(LAS3 const i32x4d*)(bp0 + (SB_(b, h) - 4 * GHTB) + _n * 8192); \
;         dst[_n].hi = *(LAS3 const i32x4d*)(bp1 + (SB_(b, h) - 4 * GHTB) + _n * 8192); } } while (0)
;     ...
;     { const int p1 = (1 < nt) ? 1 : 0; STG_B(1, 0, p1); STG_A(1, 0, p1); STG_B(1, 1, p1); }
;     G_WAIT_V(6); G_BAR;
;     for (int t = 0; t < nt; t += 2) {
;         const int t1 = (t + 1 < nt) ? t + 1 : nt - 1, t2 = (t + 2 < nt) ? t + 2 : nt - 1, t3 = (t + 3 < nt) ? t + 3 : nt - 1;
;         LDBF(B0, 0, 0); G_SCHED; LDA_(At, 0, 0); STG_A(1, 1, t1);
;         G_WAIT_L(8); G_BAR; G_WAIT_L(0); MMAD(0, 0, At, B0); G_BAR; G_SCHED;
;         LDBF(B1, 0, 1); STG_B(0, 0, t2);
;         G_BAR; G_WAIT_L(0); MMAD(0, 1, At, B1); G_BAR;
;         LDA_(At, 0, 1); STG_A(0, 0, t2);
.LBB0_469:
	s_add_u32 s25, s4, 0x8000
	s_addc_u32 s28, vcc_lo, 0
	s_add_u32 s0, s25, s91
	s_barrier
	s_addc_u32 s1, s28, s93
	s_mov_b32 m0, s60
	s_nop 0
	global_load_lds_dwordx4 v159, s[0:1]
	s_add_u32 s0, s25, s92
	s_addc_u32 s1, s28, s96
	s_mov_b32 m0, s68
	s_nop 0
	global_load_lds_dwordx4 v159, s[0:1]
	s_mov_b32 m0, s90
	s_nop 0
	global_load_lds_dwordx4 v144, s[56:57]
	s_add_u32 s25, s4, 0xc000
	s_mov_b32 m0, s88
	s_nop 0
	global_load_lds_dwordx4 v152, s[56:57]
	s_addc_u32 s28, vcc_lo, 0
	s_add_u32 s0, s25, s91
	s_addc_u32 s1, s28, s93
	s_mov_b32 m0, s33
	s_nop 0
	global_load_lds_dwordx4 v159, s[0:1]
	s_add_u32 s0, s25, s92
	s_addc_u32 s1, s28, s96
	s_mov_b32 m0, s6
	s_nop 0
	global_load_lds_dwordx4 v159, s[0:1]
	s_waitcnt vmcnt(6)
	s_barrier
	s_mov_b64 s[40:41], s[56:57]
	s_mov_b32 vcc_hi, 0
	s_mov_b64 s[0:1], s[62:63]
	v_readlane_b32 s38, v254, 62
	v_readlane_b32 s39, v254, 63
.LBB0_470:
	s_add_i32 s25, vcc_hi, 2
	s_min_u32 s28, vcc_hi, 12
	s_add_u32 s68, s0, 0x80
	s_addc_u32 s69, s1, 0
	s_and_b32 s29, s25, 14
	s_cmp_lt_u32 vcc_hi, 14
	s_cselect_b32 s29, s29, 15
	s_lshl_b32 s30, s29, 15
	s_add_u32 s30, s4, s30
	s_addc_u32 s31, vcc_lo, 0
	s_add_u32 s70, s30, s91
	s_addc_u32 s71, s31, s93
	s_add_u32 s72, s30, s92
	s_addc_u32 s73, s31, s96
	s_lshl_b32 s29, s29, 7
	s_add_u32 s56, s62, s29
	s_addc_u32 s57, s63, 0
	s_add_u32 s29, s30, 0x4000
	s_addc_u32 s30, s31, 0
	s_add_u32 s58, s29, s91
	s_addc_u32 s59, s30, s93
	s_add_u32 s60, s29, s92
	s_addc_u32 s61, s30, s96
	s_add_i32 s28, s28, 3
	s_lshl_b32 s29, s28, 15
	s_add_u32 s29, s4, s29
	s_addc_u32 s30, vcc_lo, 0
	s_add_u32 s36, s29, s91
	s_addc_u32 s37, s30, s93
	s_add_u32 s54, s29, s92
	s_addc_u32 s55, s30, s96
	s_lshl_b32 s28, s28, 7
	s_add_u32 s34, s62, s28
	s_addc_u32 s35, s63, 0
	s_add_u32 s31, s29, 0x4000
	ds_read_b128 v[0:3], v157
	ds_read_b128 v[8:11], v157 offset:8192
	ds_read_b128 v[4:7], v158
	ds_read_b128 v[12:15], v158 offset:8192
	s_addc_u32 s74, s30, 0
	s_add_u32 s28, s31, s91
	s_addc_u32 s29, s74, s93
	s_add_u32 s30, s31, s92
	s_addc_u32 s31, s74, s96
	s_add_u32 s0, s0, 0x100
	s_addc_u32 s1, s1, 0
	s_cmp_gt_u32 vcc_hi, 13
	ds_read_b128 v[160:163], v155
	ds_read_b128 v[168:171], v155 offset:2048
	ds_read_b128 v[164:167], v156
	ds_read_b128 v[172:175], v156 offset:2048
	ds_read_b128 v[176:179], v155 offset:4096
	ds_read_b128 v[184:187], v155 offset:6144
	ds_read_b128 v[180:183], v156 offset:4096
	ds_read_b128 v[188:191], v156 offset:6144
	s_mov_b32 m0, s38
	s_nop 0
	global_load_lds_dwordx4 v153, s[68:69]
	s_nop 0
	s_mov_b32 m0, s39
	s_nop 0
	global_load_lds_dwordx4 v154, s[68:69]
	s_waitcnt lgkmcnt(8)
	s_waitcnt vmcnt(10)
	s_barrier
	s_waitcnt lgkmcnt(0)
	v_readlane_b32 s69, v255, 8
	s_setprio 1
	s_waitcnt lgkmcnt(5)
	v_mfma_scale_f32_16x16x128_f8f6f4 v[140:143], v[0:7], v[160:167], v[140:143], v147, v147 op_sel:[0,1,0] op_sel_hi:[0,0,0]
	v_mfma_scale_f32_16x16x128_f8f6f4 v[132:135], v[8:15], v[160:167], v[132:135], v147, v147 op_sel:[0,1,0] op_sel_hi:[0,0,0]
	s_waitcnt lgkmcnt(4)
	v_mfma_scale_f32_16x16x128_f8f6f4 v[124:127], v[0:7], v[168:175], v[124:127], v147, v147 op_sel:[0,1,0] op_sel_hi:[0,0,0]
	v_mfma_scale_f32_16x16x128_f8f6f4 v[116:119], v[8:15], v[168:175], v[116:119], v147, v147 op_sel:[0,1,0] op_sel_hi:[0,0,0]
	s_waitcnt lgkmcnt(1)
	v_mfma_scale_f32_16x16x128_f8f6f4 v[208:211], v[0:7], v[176:183], v[108:111], v147, v147 op_sel:[0,1,0] op_sel_hi:[0,0,0]
	v_mfma_scale_f32_16x16x128_f8f6f4 v[212:215], v[8:15], v[176:183], v[100:103], v147, v147 op_sel:[0,1,0] op_sel_hi:[0,0,0]
	s_waitcnt lgkmcnt(0)
	v_mfma_scale_f32_16x16x128_f8f6f4 v[216:219], v[0:7], v[184:191], v[92:95], v147, v147 op_sel:[0,1,0] op_sel_hi:[0,0,0]
	v_mfma_scale_f32_16x16x128_f8f6f4 v[220:223], v[8:15], v[184:191], v[84:87], v147, v147 op_sel:[0,1,0] op_sel_hi:[0,0,0]
	s_setprio 0
	s_barrier
	ds_read_b128 v[192:195], v157 offset:16384
	ds_read_b128 v[200:203], v157 offset:24576
	ds_read_b128 v[196:199], v158 offset:16384
	ds_read_b128 v[204:207], v158 offset:24576
	s_mov_b32 m0, s78
	s_nop 0
	global_load_lds_dwordx4 v159, s[70:71]
	v_readlane_b32 s71, v255, 9
	s_mov_b32 m0, s69
	s_nop 0
	global_load_lds_dwordx4 v159, s[72:73]
	s_waitcnt vmcnt(10)
	s_barrier
	s_waitcnt lgkmcnt(0)
	s_setprio 1
	s_waitcnt lgkmcnt(1)
	v_mfma_scale_f32_16x16x128_f8f6f4 v[136:139], v[192:199], v[160:167], v[136:139], v147, v147 op_sel:[0,1,0] op_sel_hi:[0,0,0]
	s_waitcnt lgkmcnt(0)
	v_mfma_scale_f32_16x16x128_f8f6f4 v[128:131], v[200:207], v[160:167], v[128:131], v147, v147 op_sel:[0,1,0] op_sel_hi:[0,0,0]
	v_mfma_scale_f32_16x16x128_f8f6f4 v[120:123], v[192:199], v[168:175], v[120:123], v147, v147 op_sel:[0,1,0] op_sel_hi:[0,0,0]
	v_mfma_scale_f32_16x16x128_f8f6f4 v[112:115], v[200:207], v[168:175], v[112:115], v147, v147 op_sel:[0,1,0] op_sel_hi:[0,0,0]
	v_mfma_scale_f32_16x16x128_f8f6f4 v[224:227], v[192:199], v[176:183], v[104:107], v147, v147 op_sel:[0,1,0] op_sel_hi:[0,0,0]
	v_mfma_scale_f32_16x16x128_f8f6f4 v[176:179], v[200:207], v[176:183], v[96:99], v147, v147 op_sel:[0,1,0] op_sel_hi:[0,0,0]
	v_mfma_scale_f32_16x16x128_f8f6f4 v[180:183], v[192:199], v[184:191], v[88:91], v147, v147 op_sel:[0,1,0] op_sel_hi:[0,0,0]
	v_mfma_scale_f32_16x16x128_f8f6f4 v[184:187], v[200:207], v[184:191], v[20:23], v147, v147 op_sel:[0,1,0] op_sel_hi:[0,0,0]
	s_setprio 0
	s_barrier
	ds_read_b128 v[80:83], v155 offset:16384
	s_nop 2
	ds_read_b128 v[88:91], v155 offset:18432
	ds_read_b128 v[84:87], v156 offset:16384
	ds_read_b128 v[92:95], v156 offset:18432
	ds_read_b128 v[96:99], v155 offset:20480
	ds_read_b128 v[104:107], v155 offset:22528
	ds_read_b128 v[100:103], v156 offset:20480
	ds_read_b128 v[108:111], v156 offset:22528
	s_mov_b32 m0, s94
	s_nop 0
	global_load_lds_dwordx4 v144, s[56:57]
	s_nop 0
	s_mov_b32 m0, s83
	s_nop 0
	global_load_lds_dwordx4 v152, s[56:57]
	s_barrier
; #define G_WAIT_V(n) asm volatile("s_waitcnt vmcnt(" #n ")" ::: "memory")
; #define G_WAIT_L(n) asm volatile("s_waitcnt lgkmcnt(" #n ")" ::: "memory")
; #define G_BAR do { asm volatile("" ::: "memory"); __builtin_amdgcn_s_barrier(); asm volatile("" ::: "memory"); } while (0)
; #define G_SCHED __builtin_amdgcn_sched_barrier(0)
; #define STG_A(b, h, kt) do { const unsigned char* _g = A + (size_t)KT_(kt) * ASTEP; \
;         dma16((const void*)(_g + (size_t)((h) * 128) * ROWB), ROWB ? aoff[0][0] : aoff[h][0], lds_u + SA_(b, h) + dma0); \
;         dma16((const void*)(_g + (size_t)((h) * 128 + 64) * ROWB), ROWB ? aoff[0][0] : aoff[h][1], lds_u + SA_(b, h) + dma1); } while (0)
; #define STG_B(b, h, kt) do { const unsigned char* _g = img + (size_t)KT_(kt) * 32768 + (h) * 16384; \
;         dma16((const void*)(_g + dma0), boffl, lds_u + SB_(b, h) + dma0); \
;         dma16((const void*)(_g + dma1), boffl, lds_u + SB_(b, h) + dma1); } while (0)
; #define LDA_(dst, b, h) do { _Pragma("unroll") for (int _m = 0; _m < 4; ++_m) { \
;         dst[_m].lo = *(LAS3 const i32x4d*)(ap0 + SA_(b, h) + _m * 2048); \
;         dst[_m].hi = *(LAS3 const i32x4d*)(ap1 + SA_(b, h) + _m * 2048); } } while (0)
; #define LDBF(dst, b, h) do { _Pragma("unroll") for (int _n = 0; _n < 2; ++_n) { \
;         dst[_n].lo = *(LAS3 const i32x4d*)(bp0 + (SB_(b, h) - 4 * GHTB) + _n * 8192); \
;         dst[_n].hi = *(LAS3 const i32x4d*)(bp1 + (SB_(b, h) - 4 * GHTB) + _n * 8192); } } while (0)
;     ...
;         G_BAR; G_WAIT_L(0); MMAD(1, 0, At, B0); G_BAR; G_SCHED;
;         STG_B(0, 1, t2);
;         G_WAIT_V(6); G_BAR; MMAD(1, 1, At, B1); G_BAR;
;         LDBF(B0, 1, 0); G_SCHED; LDA_(At, 1, 0); STG_A(0, 1, t2);
;         G_WAIT_L(8); G_BAR; G_WAIT_L(0); MMAD(0, 0, At, B0); G_BAR; G_SCHED;
;         LDBF(B1, 1, 1); STG_B(1, 0, t3);
	s_waitcnt lgkmcnt(0)
	s_setprio 1
	s_waitcnt lgkmcnt(5)
	v_mfma_scale_f32_16x16x128_f8f6f4 v[76:79], v[0:7], v[80:87], v[76:79], v147, v147 op_sel:[0,1,0] op_sel_hi:[0,0,0]
	v_mfma_scale_f32_16x16x128_f8f6f4 v[68:71], v[8:15], v[80:87], v[68:71], v147, v147 op_sel:[0,1,0] op_sel_hi:[0,0,0]
	s_waitcnt lgkmcnt(4)
	v_mfma_scale_f32_16x16x128_f8f6f4 v[60:63], v[0:7], v[88:95], v[60:63], v147, v147 op_sel:[0,1,0] op_sel_hi:[0,0,0]
	v_mfma_scale_f32_16x16x128_f8f6f4 v[52:55], v[8:15], v[88:95], v[52:55], v147, v147 op_sel:[0,1,0] op_sel_hi:[0,0,0]
	s_waitcnt lgkmcnt(0)
	v_mfma_scale_f32_16x16x128_f8f6f4 v[240:243], v[8:15], v[104:111], v[240:243], v147, v147 op_sel:[0,1,0] op_sel_hi:[0,0,0]
	v_mfma_scale_f32_16x16x128_f8f6f4 v[228:231], v[0:7], v[96:103], v[44:47], v147, v147 op_sel:[0,1,0] op_sel_hi:[0,0,0]
	v_mfma_scale_f32_16x16x128_f8f6f4 v[232:235], v[8:15], v[96:103], v[36:39], v147, v147 op_sel:[0,1,0] op_sel_hi:[0,0,0]
	v_mfma_scale_f32_16x16x128_f8f6f4 v[236:239], v[0:7], v[104:111], v[28:31], v147, v147 op_sel:[0,1,0] op_sel_hi:[0,0,0]
	s_setprio 0
	s_barrier
	s_mov_b32 m0, s82
	s_nop 0
	global_load_lds_dwordx4 v159, s[58:59]
	s_mov_b32 m0, s71
	s_nop 0
	global_load_lds_dwordx4 v159, s[60:61]
	s_waitcnt vmcnt(10)
	s_barrier
	v_readlane_b32 s68, v255, 11
	v_readlane_b32 s60, v255, 10
	s_setprio 1
	v_mfma_scale_f32_16x16x128_f8f6f4 v[72:75], v[192:199], v[80:87], v[72:75], v147, v147 op_sel:[0,1,0] op_sel_hi:[0,0,0]
	v_mfma_scale_f32_16x16x128_f8f6f4 v[64:67], v[200:207], v[80:87], v[64:67], v147, v147 op_sel:[0,1,0] op_sel_hi:[0,0,0]
	v_mfma_scale_f32_16x16x128_f8f6f4 v[56:59], v[192:199], v[88:95], v[56:59], v147, v147 op_sel:[0,1,0] op_sel_hi:[0,0,0]
	v_mfma_scale_f32_16x16x128_f8f6f4 v[48:51], v[200:207], v[88:95], v[48:51], v147, v147 op_sel:[0,1,0] op_sel_hi:[0,0,0]
	v_mfma_scale_f32_16x16x128_f8f6f4 v[244:247], v[192:199], v[96:103], v[40:43], v147, v147 op_sel:[0,1,0] op_sel_hi:[0,0,0]
	v_mfma_scale_f32_16x16x128_f8f6f4 v[248:251], v[200:207], v[96:103], v[32:35], v147, v147 op_sel:[0,1,0] op_sel_hi:[0,0,0]
	v_mfma_scale_f32_16x16x128_f8f6f4 v[148:151], v[192:199], v[104:111], v[24:27], v147, v147 op_sel:[0,1,0] op_sel_hi:[0,0,0]
	v_mfma_scale_f32_16x16x128_f8f6f4 v[80:83], v[200:207], v[104:111], v[16:19], v147, v147 op_sel:[0,1,0] op_sel_hi:[0,0,0]
	s_setprio 0
	s_barrier
	ds_read_b128 v[0:3], v157 offset:32768
	ds_read_b128 v[8:11], v157 offset:40960
	ds_read_b128 v[4:7], v158 offset:32768
	ds_read_b128 v[12:15], v158 offset:40960
	s_nop 0
	ds_read_b128 v[16:19], v155 offset:32768
	ds_read_b128 v[24:27], v155 offset:34816
	ds_read_b128 v[20:23], v156 offset:32768
	ds_read_b128 v[28:31], v156 offset:34816
	ds_read_b128 v[32:35], v155 offset:36864
	ds_read_b128 v[40:43], v155 offset:38912
	ds_read_b128 v[36:39], v156 offset:36864
	ds_read_b128 v[44:47], v156 offset:38912
	s_mov_b32 m0, s79
	s_nop 0
	global_load_lds_dwordx4 v153, s[56:57]
	s_nop 0
	s_mov_b32 m0, s89
	s_nop 0
	global_load_lds_dwordx4 v154, s[56:57]
	s_waitcnt lgkmcnt(8)
	s_waitcnt vmcnt(10)
	s_barrier
	s_waitcnt lgkmcnt(0)
	s_setprio 1
	s_waitcnt lgkmcnt(5)
	v_mfma_scale_f32_16x16x128_f8f6f4 v[140:143], v[0:7], v[16:23], v[140:143], v147, v147 op_sel:[0,1,0] op_sel_hi:[0,0,0]
	v_mfma_scale_f32_16x16x128_f8f6f4 v[132:135], v[8:15], v[16:23], v[132:135], v147, v147 op_sel:[0,1,0] op_sel_hi:[0,0,0]
	s_waitcnt lgkmcnt(4)
	v_mfma_scale_f32_16x16x128_f8f6f4 v[124:127], v[0:7], v[24:31], v[124:127], v147, v147 op_sel:[0,1,0] op_sel_hi:[0,0,0]
	v_mfma_scale_f32_16x16x128_f8f6f4 v[116:119], v[8:15], v[24:31], v[116:119], v147, v147 op_sel:[0,1,0] op_sel_hi:[0,0,0]
	s_waitcnt lgkmcnt(1)
	v_mfma_scale_f32_16x16x128_f8f6f4 v[108:111], v[0:7], v[32:39], v[208:211], v147, v147 op_sel:[0,1,0] op_sel_hi:[0,0,0]
	v_mfma_scale_f32_16x16x128_f8f6f4 v[100:103], v[8:15], v[32:39], v[212:215], v147, v147 op_sel:[0,1,0] op_sel_hi:[0,0,0]
	s_waitcnt lgkmcnt(0)
	v_mfma_scale_f32_16x16x128_f8f6f4 v[92:95], v[0:7], v[40:47], v[216:219], v147, v147 op_sel:[0,1,0] op_sel_hi:[0,0,0]
	v_mfma_scale_f32_16x16x128_f8f6f4 v[84:87], v[8:15], v[40:47], v[220:223], v147, v147 op_sel:[0,1,0] op_sel_hi:[0,0,0]
	s_setprio 0
	s_barrier
	ds_read_b128 v[160:163], v157 offset:49152
	ds_read_b128 v[168:171], v157 offset:57344
	ds_read_b128 v[164:167], v158 offset:49152
	ds_read_b128 v[172:175], v158 offset:57344
	s_mov_b32 m0, s60
	s_nop 0
	global_load_lds_dwordx4 v159, s[36:37]
	s_mov_b32 m0, s68
	s_nop 0
	global_load_lds_dwordx4 v159, s[54:55]
	s_waitcnt vmcnt(10)
	s_barrier
; #define G_WAIT_V(n) asm volatile("s_waitcnt vmcnt(" #n ")" ::: "memory")
; #define G_WAIT_L(n) asm volatile("s_waitcnt lgkmcnt(" #n ")" ::: "memory")
; #define G_BAR do { asm volatile("" ::: "memory"); __builtin_amdgcn_s_barrier(); asm volatile("" ::: "memory"); } while (0)
; #define G_SCHED __builtin_amdgcn_sched_barrier(0)
; #define STG_A(b, h, kt) do { const unsigned char* _g = A + (size_t)KT_(kt) * ASTEP; \
;         dma16((const void*)(_g + (size_t)((h) * 128) * ROWB), ROWB ? aoff[0][0] : aoff[h][0], lds_u + SA_(b, h) + dma0); \
;         dma16((const void*)(_g + (size_t)((h) * 128 + 64) * ROWB), ROWB ? aoff[0][0] : aoff[h][1], lds_u + SA_(b, h) + dma1); } while (0)
; #define STG_B(b, h, kt) do { const unsigned char* _g = img + (size_t)KT_(kt) * 32768 + (h) * 16384; \
;         dma16((const void*)(_g + dma0), boffl, lds_u + SB_(b, h) + dma0); \
;         dma16((const void*)(_g + dma1), boffl, lds_u + SB_(b, h) + dma1); } while (0)
; #define LDA_(dst, b, h) do { _Pragma("unroll") for (int _m = 0; _m < 4; ++_m) { \
;         dst[_m].lo = *(LAS3 const i32x4d*)(ap0 + SA_(b, h) + _m * 2048); \
;         dst[_m].hi = *(LAS3 const i32x4d*)(ap1 + SA_(b, h) + _m * 2048); } } while (0)
;     ...
;         G_BAR; G_WAIT_L(0); MMAD(0, 1, At, B1); G_BAR;
;         LDA_(At, 1, 1); STG_A(1, 0, t3);
;         G_BAR; G_WAIT_L(0); MMAD(1, 0, At, B0); G_BAR; G_SCHED;
;         STG_B(1, 1, t3);
;         G_WAIT_V(6); G_BAR; MMAD(1, 1, At, B1); G_BAR;
;     }
;     G_WAIT_V(0); G_WAIT_L(0);
;     { int wr0 = wid >> 2; asm volatile("" : "+s"(wr0)); if (wr0 == 0) G_BAR; }
;     G_BAR;
	s_waitcnt lgkmcnt(0)
	s_setprio 1
	s_waitcnt lgkmcnt(1)
	v_mfma_scale_f32_16x16x128_f8f6f4 v[136:139], v[160:167], v[16:23], v[136:139], v147, v147 op_sel:[0,1,0] op_sel_hi:[0,0,0]
	s_waitcnt lgkmcnt(0)
	v_mfma_scale_f32_16x16x128_f8f6f4 v[128:131], v[168:175], v[16:23], v[128:131], v147, v147 op_sel:[0,1,0] op_sel_hi:[0,0,0]
	v_mfma_scale_f32_16x16x128_f8f6f4 v[120:123], v[160:167], v[24:31], v[120:123], v147, v147 op_sel:[0,1,0] op_sel_hi:[0,0,0]
	v_mfma_scale_f32_16x16x128_f8f6f4 v[112:115], v[168:175], v[24:31], v[112:115], v147, v147 op_sel:[0,1,0] op_sel_hi:[0,0,0]
	v_mfma_scale_f32_16x16x128_f8f6f4 v[104:107], v[160:167], v[32:39], v[224:227], v147, v147 op_sel:[0,1,0] op_sel_hi:[0,0,0]
	v_mfma_scale_f32_16x16x128_f8f6f4 v[96:99], v[168:175], v[32:39], v[176:179], v147, v147 op_sel:[0,1,0] op_sel_hi:[0,0,0]
	v_mfma_scale_f32_16x16x128_f8f6f4 v[88:91], v[160:167], v[40:47], v[180:183], v147, v147 op_sel:[0,1,0] op_sel_hi:[0,0,0]
	v_mfma_scale_f32_16x16x128_f8f6f4 v[20:23], v[168:175], v[40:47], v[184:187], v147, v147 op_sel:[0,1,0] op_sel_hi:[0,0,0]
	s_setprio 0
	s_barrier
	s_nop 2
	ds_read_b128 v[176:179], v155 offset:49152
	s_nop 0
	ds_read_b128 v[184:187], v155 offset:51200
	ds_read_b128 v[180:183], v156 offset:49152
	ds_read_b128 v[188:191], v156 offset:51200
	ds_read_b128 v[192:195], v155 offset:53248
	ds_read_b128 v[200:203], v155 offset:55296
	ds_read_b128 v[196:199], v156 offset:53248
	ds_read_b128 v[204:207], v156 offset:55296
	s_mov_b32 m0, s90
	s_nop 0
	global_load_lds_dwordx4 v144, s[34:35]
	s_nop 0
	s_mov_b32 m0, s88
	s_nop 0
	global_load_lds_dwordx4 v152, s[34:35]
	s_barrier
	s_waitcnt lgkmcnt(0)
	s_setprio 1
	s_waitcnt lgkmcnt(5)
	v_mfma_scale_f32_16x16x128_f8f6f4 v[76:79], v[0:7], v[176:183], v[76:79], v147, v147 op_sel:[0,1,0] op_sel_hi:[0,0,0]
	v_mfma_scale_f32_16x16x128_f8f6f4 v[68:71], v[8:15], v[176:183], v[68:71], v147, v147 op_sel:[0,1,0] op_sel_hi:[0,0,0]
	s_waitcnt lgkmcnt(4)
	v_mfma_scale_f32_16x16x128_f8f6f4 v[60:63], v[0:7], v[184:191], v[60:63], v147, v147 op_sel:[0,1,0] op_sel_hi:[0,0,0]
	v_mfma_scale_f32_16x16x128_f8f6f4 v[52:55], v[8:15], v[184:191], v[52:55], v147, v147 op_sel:[0,1,0] op_sel_hi:[0,0,0]
	s_waitcnt lgkmcnt(1)
	v_mfma_scale_f32_16x16x128_f8f6f4 v[44:47], v[0:7], v[192:199], v[228:231], v147, v147 op_sel:[0,1,0] op_sel_hi:[0,0,0]
	v_mfma_scale_f32_16x16x128_f8f6f4 v[36:39], v[8:15], v[192:199], v[232:235], v147, v147 op_sel:[0,1,0] op_sel_hi:[0,0,0]
	s_waitcnt lgkmcnt(0)
	v_mfma_scale_f32_16x16x128_f8f6f4 v[28:31], v[0:7], v[200:207], v[236:239], v147, v147 op_sel:[0,1,0] op_sel_hi:[0,0,0]
	v_mfma_scale_f32_16x16x128_f8f6f4 v[240:243], v[8:15], v[200:207], v[240:243], v147, v147 op_sel:[0,1,0] op_sel_hi:[0,0,0]
	s_setprio 0
	s_barrier
	s_mov_b32 m0, s33
	s_nop 0
	global_load_lds_dwordx4 v159, s[28:29]
	s_mov_b32 m0, s6
	s_nop 0
	global_load_lds_dwordx4 v159, s[30:31]
	s_waitcnt vmcnt(10)
	s_barrier
	s_setprio 1
	v_mfma_scale_f32_16x16x128_f8f6f4 v[72:75], v[160:167], v[176:183], v[72:75], v147, v147 op_sel:[0,1,0] op_sel_hi:[0,0,0]
	v_mfma_scale_f32_16x16x128_f8f6f4 v[64:67], v[168:175], v[176:183], v[64:67], v147, v147 op_sel:[0,1,0] op_sel_hi:[0,0,0]
	v_mfma_scale_f32_16x16x128_f8f6f4 v[56:59], v[160:167], v[184:191], v[56:59], v147, v147 op_sel:[0,1,0] op_sel_hi:[0,0,0]
	v_mfma_scale_f32_16x16x128_f8f6f4 v[48:51], v[168:175], v[184:191], v[48:51], v147, v147 op_sel:[0,1,0] op_sel_hi:[0,0,0]
	v_mfma_scale_f32_16x16x128_f8f6f4 v[40:43], v[160:167], v[192:199], v[244:247], v147, v147 op_sel:[0,1,0] op_sel_hi:[0,0,0]
	v_mfma_scale_f32_16x16x128_f8f6f4 v[32:35], v[168:175], v[192:199], v[248:251], v147, v147 op_sel:[0,1,0] op_sel_hi:[0,0,0]
	v_mfma_scale_f32_16x16x128_f8f6f4 v[24:27], v[160:167], v[200:207], v[148:151], v147, v147 op_sel:[0,1,0] op_sel_hi:[0,0,0]
	v_mfma_scale_f32_16x16x128_f8f6f4 v[16:19], v[168:175], v[200:207], v[80:83], v147, v147 op_sel:[0,1,0] op_sel_hi:[0,0,0]
	s_setprio 0
	s_barrier
	s_mov_b32 vcc_hi, s25
	s_cbranch_scc0 .LBB0_470
	s_waitcnt vmcnt(0)
	s_waitcnt lgkmcnt(0)
	s_mov_b32 s0, s77
	s_mov_b32 s70, s82
	s_mov_b32 s72, s83
	s_mov_b32 s59, s89
	s_mov_b32 s61, s79
	s_cmp_eq_u32 s0, 0
	s_cbranch_scc0 .LBB0_473
	s_barrier

; #define G_BAR do { asm volatile("" ::: "memory"); __builtin_amdgcn_s_barrier(); asm volatile("" ::: "memory"); } while (0)
; #define STG_A(b, h, kt) do { const unsigned char* _g = A + (size_t)KT_(kt) * ASTEP; \
;         dma16((const void*)(_g + (size_t)((h) * 128) * ROWB), ROWB ? aoff[0][0] : aoff[h][0], lds_u + SA_(b, h) + dma0); \
;         dma16((const void*)(_g + (size_t)((h) * 128 + 64) * ROWB), ROWB ? aoff[0][0] : aoff[h][1], lds_u + SA_(b, h) + dma1); } while (0)
; #define STG_B(b, h, kt) do { const unsigned char* _g = img + (size_t)KT_(kt) * 32768 + (h) * 16384; \
;         dma16((const void*)(_g + dma0), boffl, lds_u + SB_(b, h) + dma0); \
;         dma16((const void*)(_g + dma1), boffl, lds_u + SB_(b, h) + dma1); } while (0)
;     ...
;     STG_B(0, 0, 0); STG_A(0, 0, 0); STG_B(0, 1, 0); STG_A(0, 1, 0);
;     __builtin_amdgcn_s_waitcnt(0);
;     { int wr1 = wid >> 2; asm volatile("" : "+s"(wr1)); if (wr1 == 1) G_BAR; }
;     G_BAR;
; template <int EPI>
; __device__ __forceinline__ void gemm_tile_img(const GemmArgs& g, int pm, int pn, int e, int ebase, int ecnt, LAS3 char* lds, int wid, const unsigned char* img, const TileSync& sy, int kh = -1) {
;     ...
;     for (int h = 0; h < 2; ++h)
; #pragma unroll
;         for (int i = 0; i < 2; ++i) {
;             const int rih = (i * 8 + wid) * 8 + (lane >> 3);
;             const int chunk = (lane & 7) ^ ((rih >> 1) & 7);
;             int r = pm * 256 + h * 128 + rih;
;             unsigned grow;
;             if (EPI == 2) { if (r >= ecnt) r = ecnt - 1; grow = (unsigned)(g.list[e * T + r] >> 2); }
;             else if (EPI == 3) { grow = (unsigned)(((g.abase >> 8) + pm) * (16 * 256) + h * 128 + rih); }
;             else grow = (unsigned)r;
;             aoff[h][i] = (EPI == 3) ? (grow * 128u + (unsigned)(chunk * 16)) : (EPI >= 2) ? (grow * (unsigned)D + (unsigned)(chunk * 16)) : (grow * (unsigned)D + (unsigned)(chunk * 8)) * 2u;
;         }
.LBB0_559:
	v_writelane_b32 v255, s11, 12
	s_or_b64 exec, exec, s[30:31]
	v_lshrrev_b32_e32 v1, 3, v0
	v_readlane_b32 s0, v254, 59
	v_writelane_b32 v254, s63, 40
	s_or_b32 s4, s4, s15
	v_and_or_b32 v1, v1, 7, s0
	s_lshr_b32 s0, s73, 8
	s_add_i32 s0, s0, s63
	v_lshrrev_b32_e32 v2, 1, v1
	v_xor_b32_e32 v2, v2, v0
	s_lshl_b32 s0, s0, 19
	v_readlane_b32 s36, v254, 20
	v_lshl_add_u32 v1, v1, 7, s0
	v_lshlrev_b32_e32 v2, 4, v2
	s_movk_i32 s30, 0x70
	s_lshl_b64 s[0:1], s[4:5], 19
	v_readlane_b32 s44, v254, 28
	v_and_or_b32 v136, v2, s30, v1
	s_add_u32 s4, s44, s0
	v_and_b32_e32 v2, 15, v0
	v_lshlrev_b32_e32 v3, 3, v0
	v_readlane_b32 s0, v254, 60
	v_writelane_b32 v255, s73, 13
	v_readlane_b32 s45, v254, 29
	v_and_b32_e32 v1, 63, v0
	v_bitop3_b32 v0, v3, v0, 63 bitop3:0x78
	s_waitcnt vmcnt(14)
	v_or_b32_e32 v4, s0, v2
	v_readlane_b32 s0, v254, 61
	s_addc_u32 s25, s45, s1
	v_bitop3_b32 v3, v3, s30, v1 bitop3:0x48
	v_bitop3_b32 v0, v0, 64, v147 bitop3:0x6c
	v_lshl_add_u32 v2, v2, 7, s0
	v_readlane_b32 s0, v255, 24
	v_add_u32_e32 v137, v2, v3
	v_add_u32_e32 v138, v2, v0
	v_lshl_add_u32 v2, v4, 7, s0
	s_add_u32 s0, s4, s91
	v_add_u32_e32 v139, v2, v3
	v_add_u32_e32 v140, v2, v0
	s_addc_u32 s1, s25, s93
	s_waitcnt lgkmcnt(0)
	s_barrier
	v_lshlrev_b32_e32 v141, 4, v1
	s_mov_b32 m0, s78
	s_nop 0
	global_load_lds_dwordx4 v141, s[0:1]
	s_add_u32 s0, s4, s92
	s_addc_u32 s1, s25, s96
	s_mov_b32 m0, s69
	s_nop 0
	global_load_lds_dwordx4 v141, s[0:1]
	s_mov_b32 m0, s94
	s_nop 0
	global_load_lds_dwordx4 v136, s[64:65]
	v_readlane_b32 s38, v254, 22
	v_readlane_b32 s30, v255, 2
	v_readlane_b32 s31, v255, 3
	s_mov_b32 m0, s72
	s_nop 0
	global_load_lds_dwordx4 v136, s[30:31]
	s_add_u32 s30, s4, 0x4000
	s_addc_u32 s31, s25, 0
	s_add_u32 s0, s30, s91
	s_addc_u32 s1, s31, s93
	s_mov_b32 m0, s70
	s_nop 0
	global_load_lds_dwordx4 v141, s[0:1]
	s_add_u32 s0, s30, s92
	s_addc_u32 s1, s31, s96
	s_mov_b32 m0, s71
	s_nop 0
	global_load_lds_dwordx4 v141, s[0:1]
	s_mov_b32 s11, s62
	v_readlane_b32 s30, v255, 17
	v_readlane_b32 s31, v255, 18
	s_mov_b32 m0, s61
	s_nop 0
	global_load_lds_dwordx4 v136, s[30:31]
	v_readlane_b32 s30, v255, 19
	v_readlane_b32 s31, v255, 20
	s_mov_b32 m0, s59
	s_nop 0
	global_load_lds_dwordx4 v136, s[30:31]
	s_mov_b32 s0, s77
	v_mov_b32_e32 v8, 0
	v_mov_b32_e32 v9, v8
	v_mov_b32_e32 v10, v8
	v_mov_b32_e32 v11, v8
	v_mov_b32_e32 v12, v8
	v_mov_b32_e32 v13, v8
	v_mov_b32_e32 v14, v8
	v_mov_b32_e32 v15, v8
	v_mov_b32_e32 v16, v8
	v_mov_b32_e32 v17, v8
	v_mov_b32_e32 v18, v8
	v_mov_b32_e32 v19, v8
	v_mov_b32_e32 v20, v8
	v_mov_b32_e32 v21, v8
	v_mov_b32_e32 v22, v8
	v_mov_b32_e32 v23, v8
	v_mov_b32_e32 v32, v8
	v_mov_b32_e32 v33, v8
	v_mov_b32_e32 v34, v8
	v_mov_b32_e32 v35, v8
	v_mov_b32_e32 v36, v8
	v_mov_b32_e32 v37, v8
	v_mov_b32_e32 v38, v8
	v_mov_b32_e32 v39, v8
	v_mov_b32_e32 v48, v8
	v_mov_b32_e32 v49, v8
	v_mov_b32_e32 v50, v8
	v_mov_b32_e32 v51, v8
	v_mov_b32_e32 v56, v8
	v_mov_b32_e32 v57, v8
	v_mov_b32_e32 v58, v8
	v_mov_b32_e32 v59, v8
	v_mov_b32_e32 v24, v8
	v_mov_b32_e32 v25, v8
	v_mov_b32_e32 v26, v8
	v_mov_b32_e32 v27, v8
	v_mov_b32_e32 v28, v8
	v_mov_b32_e32 v29, v8
	v_mov_b32_e32 v30, v8
	v_mov_b32_e32 v31, v8
	v_mov_b32_e32 v40, v8
	v_mov_b32_e32 v41, v8
	v_mov_b32_e32 v42, v8
	v_mov_b32_e32 v43, v8
	v_mov_b32_e32 v44, v8
	v_mov_b32_e32 v45, v8
	v_mov_b32_e32 v46, v8
	v_mov_b32_e32 v47, v8
	v_mov_b32_e32 v52, v8
	v_mov_b32_e32 v53, v8
	v_mov_b32_e32 v54, v8
	v_mov_b32_e32 v55, v8
	v_mov_b32_e32 v60, v8
	v_mov_b32_e32 v61, v8
	v_mov_b32_e32 v62, v8
	v_mov_b32_e32 v63, v8
	v_mov_b32_e32 v64, v8
	v_mov_b32_e32 v65, v8
	v_mov_b32_e32 v66, v8
	v_mov_b32_e32 v67, v8
	v_mov_b32_e32 v68, v8
	v_mov_b32_e32 v69, v8
	v_mov_b32_e32 v70, v8
	v_mov_b32_e32 v71, v8
	v_mov_b32_e32 v72, v8
	v_mov_b32_e32 v73, v8
	v_mov_b32_e32 v74, v8
	v_mov_b32_e32 v75, v8
	v_mov_b32_e32 v76, v8
	v_mov_b32_e32 v77, v8
	v_mov_b32_e32 v78, v8
	v_mov_b32_e32 v79, v8
	v_mov_b32_e32 v80, v8
	v_mov_b32_e32 v81, v8
	v_mov_b32_e32 v82, v8
	v_mov_b32_e32 v83, v8
	v_mov_b32_e32 v88, v8
	v_mov_b32_e32 v89, v8
	v_mov_b32_e32 v90, v8
	v_mov_b32_e32 v91, v8
	v_mov_b32_e32 v96, v8
	v_mov_b32_e32 v97, v8
	v_mov_b32_e32 v98, v8
	v_mov_b32_e32 v99, v8
	v_mov_b32_e32 v104, v8
	v_mov_b32_e32 v105, v8
	v_mov_b32_e32 v106, v8
	v_mov_b32_e32 v107, v8
	v_mov_b32_e32 v112, v8
	v_mov_b32_e32 v113, v8
	v_mov_b32_e32 v114, v8
	v_mov_b32_e32 v115, v8
	v_mov_b32_e32 v120, v8
	v_mov_b32_e32 v121, v8
	v_mov_b32_e32 v122, v8
	v_mov_b32_e32 v123, v8
	v_mov_b32_e32 v84, v8
	v_mov_b32_e32 v85, v8
	v_mov_b32_e32 v86, v8
	v_mov_b32_e32 v87, v8
	v_mov_b32_e32 v92, v8
	v_mov_b32_e32 v93, v8
	v_mov_b32_e32 v94, v8
	v_mov_b32_e32 v95, v8
	v_mov_b32_e32 v100, v8
	v_mov_b32_e32 v101, v8
	v_mov_b32_e32 v102, v8
	v_mov_b32_e32 v103, v8
	v_mov_b32_e32 v108, v8
	v_mov_b32_e32 v109, v8
	v_mov_b32_e32 v110, v8
	v_mov_b32_e32 v111, v8
	v_mov_b32_e32 v116, v8
	v_mov_b32_e32 v117, v8
	v_mov_b32_e32 v118, v8
	v_mov_b32_e32 v119, v8
	v_mov_b32_e32 v124, v8
	v_mov_b32_e32 v125, v8
	v_mov_b32_e32 v126, v8
	v_mov_b32_e32 v127, v8
	v_mov_b32_e32 v128, v8
	v_mov_b32_e32 v129, v8
	v_mov_b32_e32 v130, v8
	v_mov_b32_e32 v131, v8
	v_mov_b32_e32 v132, v8
	v_mov_b32_e32 v133, v8
	v_mov_b32_e32 v134, v8
	v_mov_b32_e32 v135, v8
	s_waitcnt vmcnt(0) expcnt(0) lgkmcnt(0)
	s_mov_b32 s38, s77
	s_cmp_lg_u32 s0, 1
	v_readlane_b32 s37, v254, 21
	v_readlane_b32 s39, v254, 23
	v_readlane_b32 s40, v254, 24
	v_readlane_b32 s41, v254, 25
	v_readlane_b32 s42, v254, 26
	v_readlane_b32 s43, v254, 27
	v_readlane_b32 s46, v254, 30
	v_readlane_b32 s47, v254, 31
	v_readlane_b32 s48, v254, 32
	v_readlane_b32 s49, v254, 33
	v_readlane_b32 s50, v254, 34
	v_readlane_b32 s51, v254, 35
	s_cbranch_scc1 .LBB0_561
	s_barrier
; #define G_WAIT_V(n) asm volatile("s_waitcnt vmcnt(" #n ")" ::: "memory")
; #define G_WAIT_L(n) asm volatile("s_waitcnt lgkmcnt(" #n ")" ::: "memory")
; #define G_BAR do { asm volatile("" ::: "memory"); __builtin_amdgcn_s_barrier(); asm volatile("" ::: "memory"); } while (0)
; #define G_SCHED __builtin_amdgcn_sched_barrier(0)
; #define STG_A(b, h, kt) do { const unsigned char* _g = A + (size_t)KT_(kt) * ASTEP; \
;         dma16((const void*)(_g + (size_t)((h) * 128) * ROWB), ROWB ? aoff[0][0] : aoff[h][0], lds_u + SA_(b, h) + dma0); \
;         dma16((const void*)(_g + (size_t)((h) * 128 + 64) * ROWB), ROWB ? aoff[0][0] : aoff[h][1], lds_u + SA_(b, h) + dma1); } while (0)
; #define STG_B(b, h, kt) do { const unsigned char* _g = img + (size_t)KT_(kt) * 32768 + (h) * 16384; \
;         dma16((const void*)(_g + dma0), boffl, lds_u + SB_(b, h) + dma0); \
;         dma16((const void*)(_g + dma1), boffl, lds_u + SB_(b, h) + dma1); } while (0)
; #define LDA_(dst, b, h) do { _Pragma("unroll") for (int _m = 0; _m < 4; ++_m) { \
;         dst[_m].lo = *(LAS3 const i32x4d*)(ap0 + SA_(b, h) + _m * 2048); \
;         dst[_m].hi = *(LAS3 const i32x4d*)(ap1 + SA_(b, h) + _m * 2048); } } while (0)
; #define LDBF(dst, b, h) do { _Pragma("unroll") for (int _n = 0; _n < 2; ++_n) { \
;         dst[_n].lo = *(LAS3 const i32x4d*)(bp0 + (SB_(b, h) - 4 * GHTB) + _n * 8192); \
;         dst[_n].hi = *(LAS3 const i32x4d*)(bp1 + (SB_(b, h) - 4 * GHTB) + _n * 8192); } } while (0)
;     ...
;     { const int p1 = (1 < nt) ? 1 : 0; STG_B(1, 0, p1); STG_A(1, 0, p1); STG_B(1, 1, p1); }
;     G_WAIT_V(6); G_BAR;
;     for (int t = 0; t < nt; t += 2) {
;         const int t1 = (t + 1 < nt) ? t + 1 : nt - 1, t2 = (t + 2 < nt) ? t + 2 : nt - 1, t3 = (t + 3 < nt) ? t + 3 : nt - 1;
;         LDBF(B0, 0, 0); G_SCHED; LDA_(At, 0, 0); STG_A(1, 1, t1);
;         G_WAIT_L(8); G_BAR; G_WAIT_L(0); MMAD(0, 0, At, B0); G_BAR; G_SCHED;
;         LDBF(B1, 0, 1); STG_B(0, 0, t2);
;         G_BAR; G_WAIT_L(0); MMAD(0, 1, At, B1); G_BAR;
;         LDA_(At, 0, 1); STG_A(0, 0, t2);
.LBB0_561:
	s_add_u32 s30, s4, 0x8000
	s_addc_u32 s31, s25, 0
	s_add_u32 s0, s30, s91
	s_barrier
	s_addc_u32 s1, s31, s93
	s_mov_b32 m0, s60
	s_nop 0
	global_load_lds_dwordx4 v141, s[0:1]
	s_add_u32 s0, s30, s92
	s_addc_u32 s1, s31, s96
	s_mov_b32 m0, s68
	s_nop 0
	global_load_lds_dwordx4 v141, s[0:1]
	v_readlane_b32 s30, v255, 21
	v_readlane_b32 s31, v255, 22
	s_mov_b32 m0, s90
	s_nop 0
	global_load_lds_dwordx4 v136, s[30:31]
	v_readlane_b32 s30, v255, 25
	v_readlane_b32 s31, v255, 26
	s_mov_b32 m0, s88
	s_nop 0
	global_load_lds_dwordx4 v136, s[30:31]
	s_add_u32 s30, s4, 0xc000
	s_addc_u32 s31, s25, 0
	s_add_u32 s0, s30, s91
	s_addc_u32 s1, s31, s93
	s_mov_b32 m0, s33
	s_nop 0
	global_load_lds_dwordx4 v141, s[0:1]
	s_add_u32 s0, s30, s92
	s_addc_u32 s1, s31, s96
	s_mov_b32 m0, s6
	s_nop 0
	global_load_lds_dwordx4 v141, s[0:1]
	s_waitcnt vmcnt(6)
	s_barrier
	s_mov_b32 vcc_hi, 0
	s_mov_b64 s[0:1], 0
	v_readlane_b32 s40, v254, 62
	v_readlane_b32 s41, v254, 63
.LBB0_562:
	s_add_i32 vcc_lo, vcc_hi, 2
	s_add_u32 s30, s64, s0
	s_addc_u32 s31, s65, s1
	s_add_u32 s68, s30, 0xc000
	s_addc_u32 s69, s31, 0
	s_add_u32 s76, s30, 0xe000
	s_addc_u32 s77, s31, 0
	s_add_u32 s0, s0, 0x10000
	s_addc_u32 s1, s1, 0
	s_and_b32 s30, s0, 0x70000
	s_cmp_lt_u32 vcc_hi, 14
	s_cselect_b32 s30, s30, 0x78000
	s_add_u32 s31, s4, s30
	s_addc_u32 s34, s25, 0
	s_add_u32 s84, s31, s91
	s_addc_u32 s85, s34, s93
	s_add_u32 s80, s31, s92
	s_addc_u32 s81, s34, s96
	s_add_u32 s74, s64, s30
	s_addc_u32 s75, s65, 0
	s_add_u32 s72, s74, 0x2000
	s_addc_u32 s73, s75, 0
	s_add_u32 s30, s31, 0x4000
	s_addc_u32 s31, s34, 0
	s_add_u32 s70, s30, s91
	s_addc_u32 s71, s31, s93
	s_add_u32 s62, s30, s92
	s_addc_u32 s63, s31, s96
	s_add_u32 s60, s74, 0x4000
	s_addc_u32 s61, s75, 0
	s_add_u32 s58, s74, 0x6000
	s_addc_u32 s59, s75, 0
	s_min_u32 s30, vcc_hi, 12
	s_lshl_b32 s30, s30, 15
	s_add_i32 s30, s30, 0x18000
	s_and_b32 s30, s30, 0x78000
	s_add_u32 s31, s4, s30
	s_addc_u32 s34, s25, 0
	s_add_u32 s56, s31, s91
	s_addc_u32 s57, s34, s93
	s_add_u32 s54, s31, s92
	s_addc_u32 s55, s34, s96
	s_add_u32 s48, s64, s30
	s_addc_u32 s49, s65, 0
	s_add_u32 s36, s48, 0x2000
	ds_read_b128 v[0:3], v139
	ds_read_b128 v[148:151], v139 offset:8192
	ds_read_b128 v[4:7], v140
	ds_read_b128 v[152:155], v140 offset:8192
	s_addc_u32 s37, s49, 0
	s_add_u32 s30, s31, 0x4000
	s_addc_u32 s31, s34, 0
	s_add_u32 s34, s30, s91
	s_addc_u32 s35, s31, s93
	s_add_u32 s30, s30, s92
	s_addc_u32 s31, s31, s96
	s_cmp_gt_u32 vcc_hi, 13
	ds_read_b128 v[156:159], v137
	ds_read_b128 v[164:167], v137 offset:2048
	ds_read_b128 v[160:163], v138
	ds_read_b128 v[168:171], v138 offset:2048
	ds_read_b128 v[172:175], v137 offset:4096
	ds_read_b128 v[180:183], v137 offset:6144
	ds_read_b128 v[176:179], v138 offset:4096
	ds_read_b128 v[184:187], v138 offset:6144
	s_mov_b32 s39, s78
	s_mov_b32 m0, s40
	s_nop 0
	global_load_lds_dwordx4 v136, s[68:69]
	s_mov_b32 m0, s41
	s_nop 0
	global_load_lds_dwordx4 v136, s[76:77]
	s_waitcnt lgkmcnt(8)
	s_waitcnt vmcnt(10)
	s_barrier
	s_waitcnt lgkmcnt(0)
	v_readlane_b32 s69, v255, 8
	s_mov_b32 s78, s39
	s_setprio 1
	s_waitcnt lgkmcnt(5)
	v_mfma_scale_f32_16x16x128_f8f6f4 v[132:135], v[0:7], v[156:163], v[132:135], v144, v144 op_sel:[0,1,0] op_sel_hi:[0,0,0]
	s_waitcnt lgkmcnt(4)
	v_mfma_scale_f32_16x16x128_f8f6f4 v[116:119], v[148:155], v[164:171], v[116:119], v144, v144 op_sel:[0,1,0] op_sel_hi:[0,0,0]
	s_waitcnt lgkmcnt(1)
	v_mfma_scale_f32_16x16x128_f8f6f4 v[108:111], v[0:7], v[172:179], v[108:111], v144, v144 op_sel:[0,1,0] op_sel_hi:[0,0,0]
	v_mfma_scale_f32_16x16x128_f8f6f4 v[196:199], v[148:155], v[156:163], v[128:131], v144, v144 op_sel:[0,1,0] op_sel_hi:[0,0,0]
	v_mfma_scale_f32_16x16x128_f8f6f4 v[200:203], v[0:7], v[164:171], v[124:127], v144, v144 op_sel:[0,1,0] op_sel_hi:[0,0,0]
	v_mfma_scale_f32_16x16x128_f8f6f4 v[204:207], v[148:155], v[172:179], v[100:103], v144, v144 op_sel:[0,1,0] op_sel_hi:[0,0,0]
	s_waitcnt lgkmcnt(0)
	v_mfma_scale_f32_16x16x128_f8f6f4 v[208:211], v[0:7], v[180:187], v[92:95], v144, v144 op_sel:[0,1,0] op_sel_hi:[0,0,0]
	v_mfma_scale_f32_16x16x128_f8f6f4 v[212:215], v[148:155], v[180:187], v[84:87], v144, v144 op_sel:[0,1,0] op_sel_hi:[0,0,0]
	s_setprio 0
	s_barrier
	s_nop 0
	ds_read_b128 v[124:127], v139 offset:16384
	ds_read_b128 v[188:191], v139 offset:24576
	ds_read_b128 v[128:131], v140 offset:16384
	ds_read_b128 v[192:195], v140 offset:24576
	s_mov_b32 m0, s39
	s_nop 0
	global_load_lds_dwordx4 v141, s[84:85]
	s_nop 0
	s_mov_b32 m0, s69
	s_nop 0
	global_load_lds_dwordx4 v141, s[80:81]
	s_waitcnt vmcnt(10)
	s_barrier
	s_waitcnt lgkmcnt(0)
	s_setprio 1
	s_waitcnt lgkmcnt(1)
	v_mfma_scale_f32_16x16x128_f8f6f4 v[120:123], v[124:131], v[156:163], v[120:123], v144, v144 op_sel:[0,1,0] op_sel_hi:[0,0,0]
	s_waitcnt lgkmcnt(0)
	v_mfma_scale_f32_16x16x128_f8f6f4 v[112:115], v[188:195], v[156:163], v[112:115], v144, v144 op_sel:[0,1,0] op_sel_hi:[0,0,0]
	v_mfma_scale_f32_16x16x128_f8f6f4 v[104:107], v[124:131], v[164:171], v[104:107], v144, v144 op_sel:[0,1,0] op_sel_hi:[0,0,0]
	v_mfma_scale_f32_16x16x128_f8f6f4 v[164:167], v[188:195], v[164:171], v[96:99], v144, v144 op_sel:[0,1,0] op_sel_hi:[0,0,0]
	v_mfma_scale_f32_16x16x128_f8f6f4 v[168:171], v[124:131], v[172:179], v[88:91], v144, v144 op_sel:[0,1,0] op_sel_hi:[0,0,0]
	v_mfma_scale_f32_16x16x128_f8f6f4 v[172:175], v[188:195], v[172:179], v[80:83], v144, v144 op_sel:[0,1,0] op_sel_hi:[0,0,0]
	v_mfma_scale_f32_16x16x128_f8f6f4 v[176:179], v[124:131], v[180:187], v[76:79], v144, v144 op_sel:[0,1,0] op_sel_hi:[0,0,0]
	v_mfma_scale_f32_16x16x128_f8f6f4 v[180:183], v[188:195], v[180:187], v[72:75], v144, v144 op_sel:[0,1,0] op_sel_hi:[0,0,0]
	s_setprio 0
	s_barrier
; #define G_WAIT_V(n) asm volatile("s_waitcnt vmcnt(" #n ")" ::: "memory")
; #define G_WAIT_L(n) asm volatile("s_waitcnt lgkmcnt(" #n ")" ::: "memory")
; #define G_BAR do { asm volatile("" ::: "memory"); __builtin_amdgcn_s_barrier(); asm volatile("" ::: "memory"); } while (0)
; #define G_SCHED __builtin_amdgcn_sched_barrier(0)
; #define STG_A(b, h, kt) do { const unsigned char* _g = A + (size_t)KT_(kt) * ASTEP; \
;         dma16((const void*)(_g + (size_t)((h) * 128) * ROWB), ROWB ? aoff[0][0] : aoff[h][0], lds_u + SA_(b, h) + dma0); \
;         dma16((const void*)(_g + (size_t)((h) * 128 + 64) * ROWB), ROWB ? aoff[0][0] : aoff[h][1], lds_u + SA_(b, h) + dma1); } while (0)
; #define STG_B(b, h, kt) do { const unsigned char* _g = img + (size_t)KT_(kt) * 32768 + (h) * 16384; \
;         dma16((const void*)(_g + dma0), boffl, lds_u + SB_(b, h) + dma0); \
;         dma16((const void*)(_g + dma1), boffl, lds_u + SB_(b, h) + dma1); } while (0)
; #define LDA_(dst, b, h) do { _Pragma("unroll") for (int _m = 0; _m < 4; ++_m) { \
;         dst[_m].lo = *(LAS3 const i32x4d*)(ap0 + SA_(b, h) + _m * 2048); \
;         dst[_m].hi = *(LAS3 const i32x4d*)(ap1 + SA_(b, h) + _m * 2048); } } while (0)
; #define LDBF(dst, b, h) do { _Pragma("unroll") for (int _n = 0; _n < 2; ++_n) { \
;         dst[_n].lo = *(LAS3 const i32x4d*)(bp0 + (SB_(b, h) - 4 * GHTB) + _n * 8192); \
;         dst[_n].hi = *(LAS3 const i32x4d*)(bp1 + (SB_(b, h) - 4 * GHTB) + _n * 8192); } } while (0)
;     ...
;         LDA_(At, 0, 1); STG_A(0, 0, t2);
;         G_BAR; G_WAIT_L(0); MMAD(1, 0, At, B0); G_BAR; G_SCHED;
;         STG_B(0, 1, t2);
;         G_WAIT_V(6); G_BAR; MMAD(1, 1, At, B1); G_BAR;
;         LDBF(B0, 1, 0); G_SCHED; LDA_(At, 1, 0); STG_A(0, 1, t2);
;         G_WAIT_L(8); G_BAR; G_WAIT_L(0); MMAD(0, 0, At, B0); G_BAR; G_SCHED;
	s_nop 4
	ds_read_b128 v[72:75], v137 offset:16384
	ds_read_b128 v[80:83], v137 offset:18432
	ds_read_b128 v[76:79], v138 offset:16384
	ds_read_b128 v[84:87], v138 offset:18432
	ds_read_b128 v[88:91], v137 offset:20480
	ds_read_b128 v[96:99], v137 offset:22528
	ds_read_b128 v[92:95], v138 offset:20480
	ds_read_b128 v[100:103], v138 offset:22528
	s_mov_b32 m0, s94
	s_nop 0
	global_load_lds_dwordx4 v136, s[74:75]
	s_nop 0
	s_mov_b32 m0, s83
	s_nop 0
	global_load_lds_dwordx4 v136, s[72:73]
	s_barrier
	s_waitcnt lgkmcnt(0)
	s_setprio 1
	s_waitcnt lgkmcnt(5)
	v_mfma_scale_f32_16x16x128_f8f6f4 v[68:71], v[0:7], v[72:79], v[68:71], v144, v144 op_sel:[0,1,0] op_sel_hi:[0,0,0]
	v_mfma_scale_f32_16x16x128_f8f6f4 v[64:67], v[148:155], v[72:79], v[64:67], v144, v144 op_sel:[0,1,0] op_sel_hi:[0,0,0]
	s_waitcnt lgkmcnt(4)
	v_mfma_scale_f32_16x16x128_f8f6f4 v[60:63], v[0:7], v[80:87], v[60:63], v144, v144 op_sel:[0,1,0] op_sel_hi:[0,0,0]
	v_mfma_scale_f32_16x16x128_f8f6f4 v[52:55], v[148:155], v[80:87], v[52:55], v144, v144 op_sel:[0,1,0] op_sel_hi:[0,0,0]
	s_waitcnt lgkmcnt(1)
	v_mfma_scale_f32_16x16x128_f8f6f4 v[216:219], v[0:7], v[88:95], v[44:47], v144, v144 op_sel:[0,1,0] op_sel_hi:[0,0,0]
	v_mfma_scale_f32_16x16x128_f8f6f4 v[220:223], v[148:155], v[88:95], v[40:43], v144, v144 op_sel:[0,1,0] op_sel_hi:[0,0,0]
	s_waitcnt lgkmcnt(0)
	v_mfma_scale_f32_16x16x128_f8f6f4 v[224:227], v[0:7], v[96:103], v[28:31], v144, v144 op_sel:[0,1,0] op_sel_hi:[0,0,0]
	v_mfma_scale_f32_16x16x128_f8f6f4 v[228:231], v[148:155], v[96:103], v[24:27], v144, v144 op_sel:[0,1,0] op_sel_hi:[0,0,0]
	s_setprio 0
	s_barrier
	s_mov_b32 m0, s82
	s_nop 0
	global_load_lds_dwordx4 v141, s[70:71]
	v_readlane_b32 s71, v255, 9
	s_mov_b32 m0, s71
	s_nop 0
	global_load_lds_dwordx4 v141, s[62:63]
	s_waitcnt vmcnt(10)
	s_barrier
	v_readlane_b32 s68, v255, 11
	s_setprio 1
	v_mfma_scale_f32_16x16x128_f8f6f4 v[56:59], v[124:131], v[72:79], v[56:59], v144, v144 op_sel:[0,1,0] op_sel_hi:[0,0,0]
	v_mfma_scale_f32_16x16x128_f8f6f4 v[48:51], v[188:195], v[72:79], v[48:51], v144, v144 op_sel:[0,1,0] op_sel_hi:[0,0,0]
	v_mfma_scale_f32_16x16x128_f8f6f4 v[232:235], v[124:131], v[80:87], v[36:39], v144, v144 op_sel:[0,1,0] op_sel_hi:[0,0,0]
	v_mfma_scale_f32_16x16x128_f8f6f4 v[236:239], v[188:195], v[80:87], v[32:35], v144, v144 op_sel:[0,1,0] op_sel_hi:[0,0,0]
	v_mfma_scale_f32_16x16x128_f8f6f4 v[240:243], v[124:131], v[88:95], v[20:23], v144, v144 op_sel:[0,1,0] op_sel_hi:[0,0,0]
	v_mfma_scale_f32_16x16x128_f8f6f4 v[244:247], v[188:195], v[88:95], v[16:19], v144, v144 op_sel:[0,1,0] op_sel_hi:[0,0,0]
	v_mfma_scale_f32_16x16x128_f8f6f4 v[248:251], v[124:131], v[96:103], v[12:15], v144, v144 op_sel:[0,1,0] op_sel_hi:[0,0,0]
	v_mfma_scale_f32_16x16x128_f8f6f4 v[188:191], v[188:195], v[96:103], v[8:11], v144, v144 op_sel:[0,1,0] op_sel_hi:[0,0,0]
	s_setprio 0
	s_barrier
	ds_read_b128 v[0:3], v139 offset:32768
	s_nop 3
	ds_read_b128 v[8:11], v139 offset:40960
	ds_read_b128 v[4:7], v140 offset:32768
	ds_read_b128 v[12:15], v140 offset:40960
	ds_read_b128 v[16:19], v137 offset:32768
	ds_read_b128 v[24:27], v137 offset:34816
	ds_read_b128 v[20:23], v138 offset:32768
	ds_read_b128 v[28:31], v138 offset:34816
	ds_read_b128 v[32:35], v137 offset:36864
	ds_read_b128 v[40:43], v137 offset:38912
	ds_read_b128 v[36:39], v138 offset:36864
	ds_read_b128 v[44:47], v138 offset:38912
	s_mov_b32 m0, s79
	s_nop 0
	global_load_lds_dwordx4 v136, s[60:61]
	s_mov_b32 m0, s89
	s_nop 0
	global_load_lds_dwordx4 v136, s[58:59]
	s_waitcnt lgkmcnt(8)
	s_waitcnt vmcnt(10)
	s_barrier
	s_waitcnt lgkmcnt(0)
	v_readlane_b32 s60, v255, 10
	s_setprio 1
	s_waitcnt lgkmcnt(5)
	v_mfma_scale_f32_16x16x128_f8f6f4 v[132:135], v[0:7], v[16:23], v[132:135], v144, v144 op_sel:[0,1,0] op_sel_hi:[0,0,0]
	v_mfma_scale_f32_16x16x128_f8f6f4 v[128:131], v[8:15], v[16:23], v[196:199], v144, v144 op_sel:[0,1,0] op_sel_hi:[0,0,0]
	s_waitcnt lgkmcnt(4)
	v_mfma_scale_f32_16x16x128_f8f6f4 v[124:127], v[0:7], v[24:31], v[200:203], v144, v144 op_sel:[0,1,0] op_sel_hi:[0,0,0]
	v_mfma_scale_f32_16x16x128_f8f6f4 v[116:119], v[8:15], v[24:31], v[116:119], v144, v144 op_sel:[0,1,0] op_sel_hi:[0,0,0]
	s_waitcnt lgkmcnt(1)
	v_mfma_scale_f32_16x16x128_f8f6f4 v[108:111], v[0:7], v[32:39], v[108:111], v144, v144 op_sel:[0,1,0] op_sel_hi:[0,0,0]
	v_mfma_scale_f32_16x16x128_f8f6f4 v[100:103], v[8:15], v[32:39], v[204:207], v144, v144 op_sel:[0,1,0] op_sel_hi:[0,0,0]
	s_waitcnt lgkmcnt(0)
	v_mfma_scale_f32_16x16x128_f8f6f4 v[92:95], v[0:7], v[40:47], v[208:211], v144, v144 op_sel:[0,1,0] op_sel_hi:[0,0,0]
	v_mfma_scale_f32_16x16x128_f8f6f4 v[84:87], v[8:15], v[40:47], v[212:215], v144, v144 op_sel:[0,1,0] op_sel_hi:[0,0,0]
	s_setprio 0
	s_barrier
; #define G_WAIT_V(n) asm volatile("s_waitcnt vmcnt(" #n ")" ::: "memory")
; #define G_WAIT_L(n) asm volatile("s_waitcnt lgkmcnt(" #n ")" ::: "memory")
; #define G_BAR do { asm volatile("" ::: "memory"); __builtin_amdgcn_s_barrier(); asm volatile("" ::: "memory"); } while (0)
; #define G_SCHED __builtin_amdgcn_sched_barrier(0)
; #define STG_A(b, h, kt) do { const unsigned char* _g = A + (size_t)KT_(kt) * ASTEP; \
;         dma16((const void*)(_g + (size_t)((h) * 128) * ROWB), ROWB ? aoff[0][0] : aoff[h][0], lds_u + SA_(b, h) + dma0); \
;         dma16((const void*)(_g + (size_t)((h) * 128 + 64) * ROWB), ROWB ? aoff[0][0] : aoff[h][1], lds_u + SA_(b, h) + dma1); } while (0)
; #define STG_B(b, h, kt) do { const unsigned char* _g = img + (size_t)KT_(kt) * 32768 + (h) * 16384; \
;         dma16((const void*)(_g + dma0), boffl, lds_u + SB_(b, h) + dma0); \
;         dma16((const void*)(_g + dma1), boffl, lds_u + SB_(b, h) + dma1); } while (0)
; #define LDA_(dst, b, h) do { _Pragma("unroll") for (int _m = 0; _m < 4; ++_m) { \
;         dst[_m].lo = *(LAS3 const i32x4d*)(ap0 + SA_(b, h) + _m * 2048); \
;         dst[_m].hi = *(LAS3 const i32x4d*)(ap1 + SA_(b, h) + _m * 2048); } } while (0)
; #define LDBF(dst, b, h) do { _Pragma("unroll") for (int _n = 0; _n < 2; ++_n) { \
;         dst[_n].lo = *(LAS3 const i32x4d*)(bp0 + (SB_(b, h) - 4 * GHTB) + _n * 8192); \
;         dst[_n].hi = *(LAS3 const i32x4d*)(bp1 + (SB_(b, h) - 4 * GHTB) + _n * 8192); } } while (0)
;     ...
;         LDBF(B1, 1, 1); STG_B(1, 0, t3);
;         G_BAR; G_WAIT_L(0); MMAD(0, 1, At, B1); G_BAR;
;         LDA_(At, 1, 1); STG_A(1, 0, t3);
;         G_BAR; G_WAIT_L(0); MMAD(1, 0, At, B0); G_BAR; G_SCHED;
;         STG_B(1, 1, t3);
;         G_WAIT_V(6); G_BAR; MMAD(1, 1, At, B1); G_BAR;
;     }
;     G_WAIT_V(0); G_WAIT_L(0);
;     { int wr0 = wid >> 2; asm volatile("" : "+s"(wr0)); if (wr0 == 0) G_BAR; }
;     G_BAR;
	ds_read_b128 v[148:151], v139 offset:49152
	ds_read_b128 v[156:159], v139 offset:57344
	ds_read_b128 v[152:155], v140 offset:49152
	ds_read_b128 v[160:163], v140 offset:57344
	s_mov_b32 m0, s60
	s_nop 0
	global_load_lds_dwordx4 v141, s[56:57]
	s_mov_b32 m0, s68
	s_nop 0
	global_load_lds_dwordx4 v141, s[54:55]
	s_waitcnt vmcnt(10)
	s_barrier
	s_waitcnt lgkmcnt(0)
	s_setprio 1
	s_waitcnt lgkmcnt(1)
	v_mfma_scale_f32_16x16x128_f8f6f4 v[120:123], v[148:155], v[16:23], v[120:123], v144, v144 op_sel:[0,1,0] op_sel_hi:[0,0,0]
	s_waitcnt lgkmcnt(0)
	v_mfma_scale_f32_16x16x128_f8f6f4 v[112:115], v[156:163], v[16:23], v[112:115], v144, v144 op_sel:[0,1,0] op_sel_hi:[0,0,0]
	v_mfma_scale_f32_16x16x128_f8f6f4 v[104:107], v[148:155], v[24:31], v[104:107], v144, v144 op_sel:[0,1,0] op_sel_hi:[0,0,0]
	v_mfma_scale_f32_16x16x128_f8f6f4 v[96:99], v[156:163], v[24:31], v[164:167], v144, v144 op_sel:[0,1,0] op_sel_hi:[0,0,0]
	v_mfma_scale_f32_16x16x128_f8f6f4 v[88:91], v[148:155], v[32:39], v[168:171], v144, v144 op_sel:[0,1,0] op_sel_hi:[0,0,0]
	v_mfma_scale_f32_16x16x128_f8f6f4 v[80:83], v[156:163], v[32:39], v[172:175], v144, v144 op_sel:[0,1,0] op_sel_hi:[0,0,0]
	v_mfma_scale_f32_16x16x128_f8f6f4 v[76:79], v[148:155], v[40:47], v[176:179], v144, v144 op_sel:[0,1,0] op_sel_hi:[0,0,0]
	v_mfma_scale_f32_16x16x128_f8f6f4 v[72:75], v[156:163], v[40:47], v[180:183], v144, v144 op_sel:[0,1,0] op_sel_hi:[0,0,0]
	s_setprio 0
	s_barrier
	ds_read_b128 v[16:19], v137 offset:49152
	ds_read_b128 v[164:167], v137 offset:51200
	ds_read_b128 v[20:23], v138 offset:49152
	ds_read_b128 v[168:171], v138 offset:51200
	ds_read_b128 v[172:175], v137 offset:53248
	ds_read_b128 v[180:183], v137 offset:55296
	ds_read_b128 v[176:179], v138 offset:53248
	ds_read_b128 v[184:187], v138 offset:55296
	s_mov_b32 m0, s90
	s_nop 0
	global_load_lds_dwordx4 v136, s[48:49]
	s_mov_b32 m0, s88
	s_nop 0
	global_load_lds_dwordx4 v136, s[36:37]
	s_barrier
	s_waitcnt lgkmcnt(0)
	s_setprio 1
	s_waitcnt lgkmcnt(5)
	v_mfma_scale_f32_16x16x128_f8f6f4 v[68:71], v[0:7], v[16:23], v[68:71], v144, v144 op_sel:[0,1,0] op_sel_hi:[0,0,0]
	v_mfma_scale_f32_16x16x128_f8f6f4 v[64:67], v[8:15], v[16:23], v[64:67], v144, v144 op_sel:[0,1,0] op_sel_hi:[0,0,0]
	s_waitcnt lgkmcnt(4)
	v_mfma_scale_f32_16x16x128_f8f6f4 v[60:63], v[0:7], v[164:171], v[60:63], v144, v144 op_sel:[0,1,0] op_sel_hi:[0,0,0]
	v_mfma_scale_f32_16x16x128_f8f6f4 v[52:55], v[8:15], v[164:171], v[52:55], v144, v144 op_sel:[0,1,0] op_sel_hi:[0,0,0]
	s_waitcnt lgkmcnt(1)
	v_mfma_scale_f32_16x16x128_f8f6f4 v[44:47], v[0:7], v[172:179], v[216:219], v144, v144 op_sel:[0,1,0] op_sel_hi:[0,0,0]
	v_mfma_scale_f32_16x16x128_f8f6f4 v[40:43], v[8:15], v[172:179], v[220:223], v144, v144 op_sel:[0,1,0] op_sel_hi:[0,0,0]
	s_waitcnt lgkmcnt(0)
	v_mfma_scale_f32_16x16x128_f8f6f4 v[28:31], v[0:7], v[180:187], v[224:227], v144, v144 op_sel:[0,1,0] op_sel_hi:[0,0,0]
	v_mfma_scale_f32_16x16x128_f8f6f4 v[24:27], v[8:15], v[180:187], v[228:231], v144, v144 op_sel:[0,1,0] op_sel_hi:[0,0,0]
	s_setprio 0
	s_barrier
	s_mov_b32 m0, s33
	s_nop 0
	global_load_lds_dwordx4 v141, s[34:35]
	s_mov_b32 m0, s6
	s_nop 0
	global_load_lds_dwordx4 v141, s[30:31]
	s_waitcnt vmcnt(10)
	s_barrier
	s_setprio 1
	v_mfma_scale_f32_16x16x128_f8f6f4 v[56:59], v[148:155], v[16:23], v[56:59], v144, v144 op_sel:[0,1,0] op_sel_hi:[0,0,0]
	v_mfma_scale_f32_16x16x128_f8f6f4 v[48:51], v[156:163], v[16:23], v[48:51], v144, v144 op_sel:[0,1,0] op_sel_hi:[0,0,0]
	v_mfma_scale_f32_16x16x128_f8f6f4 v[36:39], v[148:155], v[164:171], v[232:235], v144, v144 op_sel:[0,1,0] op_sel_hi:[0,0,0]
	v_mfma_scale_f32_16x16x128_f8f6f4 v[32:35], v[156:163], v[164:171], v[236:239], v144, v144 op_sel:[0,1,0] op_sel_hi:[0,0,0]
	v_mfma_scale_f32_16x16x128_f8f6f4 v[20:23], v[148:155], v[172:179], v[240:243], v144, v144 op_sel:[0,1,0] op_sel_hi:[0,0,0]
	v_mfma_scale_f32_16x16x128_f8f6f4 v[16:19], v[156:163], v[172:179], v[244:247], v144, v144 op_sel:[0,1,0] op_sel_hi:[0,0,0]
	v_mfma_scale_f32_16x16x128_f8f6f4 v[12:15], v[148:155], v[180:187], v[248:251], v144, v144 op_sel:[0,1,0] op_sel_hi:[0,0,0]
	v_mfma_scale_f32_16x16x128_f8f6f4 v[8:11], v[156:163], v[180:187], v[188:191], v144, v144 op_sel:[0,1,0] op_sel_hi:[0,0,0]
	s_setprio 0
	s_barrier
	s_mov_b32 vcc_hi, vcc_lo
	s_cbranch_scc0 .LBB0_562
	s_waitcnt vmcnt(0)
	s_waitcnt lgkmcnt(0)
	s_mov_b32 s0, s38
	s_mov_b32 s72, s83
	s_mov_b32 s70, s82
	s_mov_b32 s61, s79
	s_mov_b32 s59, s89
	s_mov_b32 s77, s38
	s_cmp_eq_u32 s0, 0
	s_cbranch_scc0 .LBB0_565
	s_barrier
